# nt (non-temporal) cache policy on the 80 global_store_dwordx4 of the four GEMM epilogues (Z, X/XN, H, X): keeps operand tiles in L2
# speedup vs baseline: 1.2140x; 1.2140x over previous
.LBB0_328:
	s_lshr_b32 s0, s8, 4
	s_and_b32 s4, s0, 0xfc
	s_ashr_i32 s0, s2, 31
	s_lshr_b32 s0, s0, 28
	s_add_i32 s0, s2, s0
	s_ashr_i32 s13, s0, 4
	v_add_u32_e32 v144, v204, v201
	s_movk_i32 s0, 0x300
	v_mul_lo_u32 v144, v144, s0
	v_sub_u32_e32 v144, v193, v144
	v_cndmask_b32_e64 v146, v203, v144, s[42:43]
	v_lshrrev_b32_e32 v144, 7, v146
	v_mad_u64_u32 v[144:145], s[0:1], v202, s13, v[144:145]
	v_lshlrev_b32_e32 v145, 4, v146
	v_lshl_add_u32 v144, v144, 19, v200
	v_and_b32_e32 v145, 0x600, v145
	v_and_b32_e32 v146, 31, v146
	v_or3_b32 v146, v144, v145, v146
	v_add_u32_e32 v144, 0xfffff200, v193
	v_mul_hi_i32 v145, v144, s6
	v_lshrrev_b32_e32 v147, 31, v145
	v_ashrrev_i32_e32 v145, 6, v145
	v_add_u32_e32 v145, v145, v147
	v_mul_i32_i24_e32 v147, 0x180, v145
	v_sub_u32_e32 v144, v144, v147
	v_mul_i32_i24_e32 v147, 0x2aab, v144
	v_mov_b32_e32 v148, 4
	v_ashrrev_i16_sdwa v148, v148, v147 dst_sel:DWORD dst_unused:UNUSED_PAD src0_sel:DWORD src1_sel:WORD_1
	v_lshrrev_b32_e32 v147, 31, v147
	v_add_u16_e32 v147, v148, v147
	v_mul_lo_u16_e32 v148, 0x60, v147
	v_sub_u16_e32 v144, v144, v148
	s_lshl_b32 s5, s13, 2
	v_bfe_i32 v148, v144, 0, 16
	v_mul_i32_i24_e32 v144, 0x600000, v145
	v_and_or_b32 v144, v148, 31, v144
	v_add_u32_e32 v145, s5, v147
	s_mov_b32 s0, 0x60000
	v_lshlrev_b32_e32 v147, 4, v148
	v_mad_u64_u32 v[144:145], s[0:1], v145, s0, v[144:145]
	v_and_b32_e32 v147, 0xfffffe00, v147
	s_mov_b32 s0, 0x3800000
	v_add3_u32 v147, v144, v147, s0
	v_add_u32_e32 v144, 0xffffef00, v193
	v_mul_hi_i32 v145, v144, s6
	v_lshrrev_b32_e32 v148, 31, v145
	v_ashrrev_i32_e32 v145, 7, v145
	v_add_u32_e32 v145, v145, v148
	v_mul_i32_i24_e32 v148, 0x300, v145
	v_sub_u32_e32 v144, v144, v148
	v_mul_i32_i24_e32 v148, 0x2aab, v144
	v_mov_b32_e32 v149, 5
	v_ashrrev_i16_sdwa v149, v149, v148 dst_sel:DWORD dst_unused:UNUSED_PAD src0_sel:DWORD src1_sel:WORD_1
	v_lshrrev_b32_e32 v148, 31, v148
	v_add_u16_e32 v148, v149, v148
	v_mul_lo_u16_e32 v149, 0xc0, v148
	v_sub_u16_e32 v144, v144, v149
	s_mov_b32 s0, 0xc00000
	v_bfe_i32 v149, v144, 0, 16
	v_mul_lo_u32 v144, v145, s0
	v_and_or_b32 v144, v149, 31, v144
	v_add_u32_e32 v145, s5, v148
	s_mov_b32 s0, 0xc0000
	v_lshlrev_b32_e32 v148, 4, v149
	v_mad_u64_u32 v[144:145], s[0:1], v145, s0, v[144:145]
	v_and_b32_e32 v148, 0xfffffe00, v148
	s_mov_b32 s0, 0x4400000
	v_add3_u32 v144, v144, v148, s0
	s_movk_i32 s0, 0xe00
	s_lshl_b32 s2, s13, 16
	v_cmp_gt_i32_e32 vcc, s0, v193
	s_movk_i32 s0, 0x1710
	s_add_i32 s2, s2, 0x5bfe900
	v_cmp_gt_u32_e64 s[42:43], s0, v193
	s_movk_i32 s0, 0x1700
	v_add_u32_e32 v145, s2, v193
	v_cndmask_b32_e64 v149, 0, v237, s[42:43]
	v_cmp_gt_i32_e64 s[46:47], s0, v193
	s_movk_i32 s0, 0x1100
	v_cndmask_b32_e32 v148, v236, v218, vcc
	v_cndmask_b32_e64 v149, v149, v239, s[46:47]
	v_cmp_gt_i32_e64 s[42:43], s0, v193
	v_cndmask_b32_e64 v144, v145, v144, s[46:47]
	s_nop 0
	v_cndmask_b32_e64 v159, v149, v148, s[42:43]
	v_cndmask_b32_e64 v144, v144, v147, s[42:43]
	v_cndmask_b32_e32 v181, v144, v146, vcc
	v_cvt_pk_bf16_f32 v144, v156, v179
	v_cvt_pk_bf16_f32 v145, v180, v182
	v_cmp_ne_u32_e64 s[42:43], 0, v159
	v_cndmask_b32_e64 v180, 4, 5, s[46:47]
	v_cvt_pk_bf16_f32 v146, v178, v185
	v_cvt_pk_bf16_f32 v147, v186, v188
	s_and_saveexec_b64 s[0:1], s[42:43]
	s_cbranch_execz .LBB0_330
	v_mul_u32_u24_e32 v148, s4, v159
	v_lshl_or_b32 v148, v192, v180, v148
	v_add_u32_e32 v212, v148, v181
	v_lshl_add_u64 v[148:149], v[212:213], 1, s[52:53]
	global_store_dwordx4 v[148:149], v[144:147], off nt

.LBB0_336:
	v_add_u32_e32 v132, v198, v197
	s_movk_i32 s0, 0x300
	v_mul_lo_u32 v132, v132, s0
	v_sub_u32_e32 v132, v194, v132
	v_cndmask_b32_e64 v134, v199, v132, s[44:45]
	v_lshrrev_b32_e32 v132, 7, v134
	v_mad_u64_u32 v[132:133], s[0:1], v195, s13, v[132:133]
	v_lshlrev_b32_e32 v133, 4, v134
	v_lshl_add_u32 v132, v132, 19, v196
	v_and_b32_e32 v133, 0x600, v133
	v_and_b32_e32 v134, 31, v134
	v_or3_b32 v134, v132, v133, v134
	v_add_u32_e32 v132, 0xfffff280, v193
	v_mul_hi_i32 v133, v132, s6
	v_lshrrev_b32_e32 v135, 31, v133
	v_ashrrev_i32_e32 v133, 6, v133
	v_add_u32_e32 v133, v133, v135
	v_mul_i32_i24_e32 v135, 0x180, v133
	v_sub_u32_e32 v132, v132, v135
	v_mul_i32_i24_e32 v135, 0x2aab, v132
	v_lshrrev_b32_e32 v136, 31, v135
	v_ashrrev_i32_e32 v135, 20, v135
	v_add_u16_e32 v135, v135, v136
	v_mul_lo_u16_e32 v136, 0x60, v135
	v_sub_u16_e32 v132, v132, v136
	v_bfe_i32 v136, v132, 0, 16
	v_mul_i32_i24_e32 v132, 0x600000, v133
	v_and_or_b32 v132, v136, 31, v132
	v_add_u32_e32 v133, s5, v135
	s_mov_b32 s0, 0x60000
	v_lshlrev_b32_e32 v135, 4, v136
	v_mad_u64_u32 v[132:133], s[0:1], v133, s0, v[132:133]
	v_and_b32_e32 v135, 0xfffffe00, v135
	s_mov_b32 s0, 0x3800000
	v_add3_u32 v135, v132, v135, s0
	v_add_u32_e32 v132, 0xffffef80, v193
	v_mul_hi_i32 v133, v132, s6
	v_lshrrev_b32_e32 v136, 31, v133
	v_ashrrev_i32_e32 v133, 7, v133
	v_add_u32_e32 v133, v133, v136
	v_mul_i32_i24_e32 v136, 0x300, v133
	v_sub_u32_e32 v132, v132, v136
	v_mul_i32_i24_e32 v136, 0x2aab, v132
	v_lshrrev_b32_e32 v137, 31, v136
	v_ashrrev_i32_e32 v136, 21, v136
	v_add_u16_e32 v136, v136, v137
	v_mul_lo_u16_e32 v137, 0xc0, v136
	v_sub_u16_e32 v132, v132, v137
	s_mov_b32 s0, 0xc00000
	v_bfe_i32 v137, v132, 0, 16
	v_mul_lo_u32 v132, v133, s0
	v_and_or_b32 v132, v137, 31, v132
	v_add_u32_e32 v133, s5, v136
	s_mov_b32 s0, 0xc0000
	v_lshlrev_b32_e32 v136, 4, v137
	v_mad_u64_u32 v[132:133], s[0:1], v133, s0, v[132:133]
	v_and_b32_e32 v136, 0xfffffe00, v136
	s_mov_b32 s0, 0x4400000
	v_add3_u32 v132, v132, v136, s0
	s_movk_i32 s0, 0xd80
	v_cmp_gt_i32_e32 vcc, s0, v193
	s_movk_i32 s0, 0x1710
	v_cmp_gt_u32_e64 s[44:45], s0, v194
	s_movk_i32 s0, 0x1680
	v_add_u32_e32 v133, s2, v194
	v_cndmask_b32_e64 v137, 0, v237, s[44:45]
	v_cmp_gt_i32_e64 s[46:47], s0, v193
	s_movk_i32 s0, 0x1080
	v_cndmask_b32_e32 v136, v236, v218, vcc
	v_cndmask_b32_e64 v137, v137, v239, s[46:47]
	v_cmp_gt_i32_e64 s[44:45], s0, v193
	v_cndmask_b32_e64 v132, v133, v132, s[46:47]
	s_nop 0
	v_cndmask_b32_e64 v158, v137, v136, s[44:45]
	v_cndmask_b32_e64 v132, v132, v135, s[44:45]
	v_cndmask_b32_e32 v172, v132, v134, vcc
	v_cvt_pk_bf16_f32 v132, v144, v145
	v_cmp_ne_u32_e64 s[44:45], 0, v158
	v_cndmask_b32_e64 v145, 4, 5, s[46:47]
	v_cvt_pk_bf16_f32 v133, v146, v148
	v_cvt_pk_bf16_f32 v134, v147, v151
	v_cvt_pk_bf16_f32 v135, v178, v156
	s_and_saveexec_b64 s[0:1], s[44:45]
	s_cbranch_execz .LBB0_338
	v_mul_u32_u24_e32 v136, s4, v158
	v_lshl_or_b32 v136, v192, v145, v136
	v_add_u32_e32 v212, v136, v172
	v_lshl_add_u64 v[136:137], v[212:213], 1, s[52:53]
	global_store_dwordx4 v[136:137], v[132:135], off nt

.LBB0_346:
	s_or_b32 s2, s4, 1
	v_cvt_pk_bf16_f32 v124, v134, v147
	v_cvt_pk_bf16_f32 v125, v148, v150
	v_cvt_pk_bf16_f32 v126, v146, v153
	v_cvt_pk_bf16_f32 v127, v154, v156
	s_and_saveexec_b64 s[0:1], s[42:43]
	s_cbranch_execz .LBB0_348
	v_mul_u32_u24_e32 v128, s2, v159
	v_lshlrev_b32_e32 v129, v180, v192
	v_add3_u32 v212, v128, v129, v181
	v_lshl_add_u64 v[128:129], v[212:213], 1, s[52:53]
	global_store_dwordx4 v[128:129], v[124:127], off nt

.LBB0_354:
	v_cvt_pk_bf16_f32 v112, v124, v125
	v_cvt_pk_bf16_f32 v113, v126, v128
	v_cvt_pk_bf16_f32 v114, v127, v131
	v_cvt_pk_bf16_f32 v115, v146, v134
	s_and_saveexec_b64 s[0:1], s[44:45]
	s_cbranch_execz .LBB0_356
	v_mul_u32_u24_e32 v116, s2, v158
	v_lshlrev_b32_e32 v117, v145, v192
	v_add3_u32 v212, v116, v117, v172
	v_lshl_add_u64 v[116:117], v[212:213], 1, s[52:53]
	global_store_dwordx4 v[116:117], v[112:115], off nt

.LBB0_364:
	s_or_b32 s2, s4, 2
	v_cvt_pk_bf16_f32 v104, v114, v127
	v_cvt_pk_bf16_f32 v105, v128, v130
	v_cvt_pk_bf16_f32 v106, v125, v133
	v_cvt_pk_bf16_f32 v107, v134, v136
	s_and_saveexec_b64 s[0:1], s[42:43]
	s_cbranch_execz .LBB0_366
	v_mul_u32_u24_e32 v108, s2, v159
	v_lshl_or_b32 v108, v192, v180, v108
	v_add_u32_e32 v212, v108, v181
	v_lshl_add_u64 v[108:109], v[212:213], 1, s[52:53]
	global_store_dwordx4 v[108:109], v[104:107], off nt

.LBB0_372:
	v_cvt_pk_bf16_f32 v92, v104, v105
	v_cvt_pk_bf16_f32 v93, v106, v108
	v_cvt_pk_bf16_f32 v94, v107, v111
	v_cvt_pk_bf16_f32 v95, v126, v114
	s_and_saveexec_b64 s[0:1], s[44:45]
	s_cbranch_execz .LBB0_374
	v_mul_u32_u24_e32 v96, s2, v158
	v_lshl_or_b32 v96, v192, v145, v96
	v_add_u32_e32 v212, v96, v172
	v_lshl_add_u64 v[96:97], v[212:213], 1, s[52:53]
	global_store_dwordx4 v[96:97], v[92:95], off nt

.LBB0_382:
	s_or_b32 s2, s4, 3
	v_cvt_pk_bf16_f32 v84, v94, v107
	v_cvt_pk_bf16_f32 v85, v108, v110
	v_cvt_pk_bf16_f32 v86, v105, v113
	v_cvt_pk_bf16_f32 v87, v114, v116
	s_and_saveexec_b64 s[0:1], s[42:43]
	s_cbranch_execz .LBB0_384
	v_mul_u32_u24_e32 v88, s2, v159
	v_lshlrev_b32_e32 v89, v180, v192
	v_add3_u32 v212, v88, v89, v181
	v_lshl_add_u64 v[88:89], v[212:213], 1, s[52:53]
	global_store_dwordx4 v[88:89], v[84:87], off nt

.LBB0_390:
	v_cvt_pk_bf16_f32 v72, v84, v85
	v_cvt_pk_bf16_f32 v73, v86, v88
	v_cvt_pk_bf16_f32 v74, v87, v91
	v_cvt_pk_bf16_f32 v75, v106, v94
	s_and_saveexec_b64 s[0:1], s[44:45]
	s_cbranch_execz .LBB0_392
	v_mul_u32_u24_e32 v76, s2, v158
	v_lshlrev_b32_e32 v77, v145, v192
	v_add3_u32 v212, v76, v77, v172
	v_lshl_add_u64 v[76:77], v[212:213], 1, s[52:53]
	global_store_dwordx4 v[76:77], v[72:75], off nt

.LBB0_400:
	s_addk_i32 s8, 0x80
	s_lshr_b32 s0, s8, 4
	s_and_b32 s2, s0, 0xfc
	v_cvt_pk_bf16_f32 v64, v74, v87
	v_cvt_pk_bf16_f32 v65, v88, v90
	v_cvt_pk_bf16_f32 v66, v85, v93
	v_cvt_pk_bf16_f32 v67, v94, v96
	s_and_saveexec_b64 s[0:1], s[42:43]
	s_cbranch_execz .LBB0_402
	v_mul_u32_u24_e32 v68, s2, v159
	v_lshl_or_b32 v68, v192, v180, v68
	v_add_u32_e32 v212, v68, v181
	v_lshl_add_u64 v[68:69], v[212:213], 1, s[52:53]
	global_store_dwordx4 v[68:69], v[64:67], off nt

.LBB0_408:
	v_cvt_pk_bf16_f32 v52, v64, v65
	v_cvt_pk_bf16_f32 v53, v66, v68
	v_cvt_pk_bf16_f32 v54, v67, v71
	v_cvt_pk_bf16_f32 v55, v86, v74
	s_and_saveexec_b64 s[0:1], s[44:45]
	s_cbranch_execz .LBB0_410
	v_mul_u32_u24_e32 v56, s2, v158
	v_lshl_or_b32 v56, v192, v145, v56
	v_add_u32_e32 v212, v56, v172
	v_lshl_add_u64 v[56:57], v[212:213], 1, s[52:53]
	global_store_dwordx4 v[56:57], v[52:55], off nt

.LBB0_418:
	s_or_b32 s4, s2, 1
	v_cvt_pk_bf16_f32 v44, v54, v67
	v_cvt_pk_bf16_f32 v45, v68, v70
	v_cvt_pk_bf16_f32 v46, v65, v73
	v_cvt_pk_bf16_f32 v47, v74, v76
	s_and_saveexec_b64 s[0:1], s[42:43]
	s_cbranch_execz .LBB0_420
	v_mul_u32_u24_e32 v48, s4, v159
	v_lshlrev_b32_e32 v49, v180, v192
	v_add3_u32 v212, v48, v49, v181
	v_lshl_add_u64 v[48:49], v[212:213], 1, s[52:53]
	global_store_dwordx4 v[48:49], v[44:47], off nt

.LBB0_426:
	v_cvt_pk_bf16_f32 v32, v44, v45
	v_cvt_pk_bf16_f32 v33, v46, v48
	v_cvt_pk_bf16_f32 v34, v47, v51
	v_cvt_pk_bf16_f32 v35, v66, v54
	s_and_saveexec_b64 s[0:1], s[44:45]
	s_cbranch_execz .LBB0_428
	v_mul_u32_u24_e32 v36, s4, v158
	v_lshlrev_b32_e32 v37, v145, v192
	v_add3_u32 v212, v36, v37, v172
	v_lshl_add_u64 v[36:37], v[212:213], 1, s[52:53]
	global_store_dwordx4 v[36:37], v[32:35], off nt

.LBB0_436:
	s_or_b32 s4, s2, 2
	v_cvt_pk_bf16_f32 v24, v34, v47
	v_cvt_pk_bf16_f32 v25, v48, v50
	v_cvt_pk_bf16_f32 v26, v45, v53
	v_cvt_pk_bf16_f32 v27, v54, v56
	s_and_saveexec_b64 s[0:1], s[42:43]
	s_cbranch_execz .LBB0_438
	v_mul_u32_u24_e32 v28, s4, v159
	v_lshl_or_b32 v28, v192, v180, v28
	v_add_u32_e32 v212, v28, v181
	v_lshl_add_u64 v[28:29], v[212:213], 1, s[52:53]
	global_store_dwordx4 v[28:29], v[24:27], off nt

.LBB0_444:
	v_cvt_pk_bf16_f32 v16, v24, v25
	v_cvt_pk_bf16_f32 v17, v26, v28
	v_cvt_pk_bf16_f32 v18, v27, v31
	v_cvt_pk_bf16_f32 v19, v46, v34
	s_and_saveexec_b64 s[0:1], s[44:45]
	s_cbranch_execz .LBB0_446
	v_mul_u32_u24_e32 v20, s4, v158
	v_lshl_or_b32 v20, v192, v145, v20
	v_add_u32_e32 v212, v20, v172
	v_lshl_add_u64 v[20:21], v[212:213], 1, s[52:53]
	global_store_dwordx4 v[20:21], v[16:19], off nt

.LBB0_454:
	s_or_b32 s2, s2, 3
	v_cvt_pk_bf16_f32 v8, v18, v27
	v_cvt_pk_bf16_f32 v9, v28, v30
	v_cvt_pk_bf16_f32 v10, v25, v33
	v_cvt_pk_bf16_f32 v11, v34, v36
	s_and_saveexec_b64 s[0:1], s[42:43]
	s_cbranch_execz .LBB0_456
	v_mul_u32_u24_e32 v12, s2, v159
	v_lshlrev_b32_e32 v13, v180, v192
	v_add3_u32 v212, v12, v13, v181
	v_lshl_add_u64 v[12:13], v[212:213], 1, s[52:53]
	global_store_dwordx4 v[12:13], v[8:11], off nt

.LBB0_462:
	v_cvt_pk_bf16_f32 v0, v8, v9
	v_cvt_pk_bf16_f32 v1, v10, v12
	v_cvt_pk_bf16_f32 v2, v11, v15
	v_cvt_pk_bf16_f32 v3, v26, v18
	s_and_saveexec_b64 s[0:1], s[44:45]
	s_cbranch_execz .LBB0_464
	v_mul_u32_u24_e32 v4, s2, v158
	v_lshlrev_b32_e32 v5, v145, v192
	v_add3_u32 v212, v4, v5, v172
	v_lshl_add_u64 v[4:5], v[212:213], 1, s[52:53]
	global_store_dwordx4 v[4:5], v[0:3], off nt

.LBB0_1058:
	s_mov_b32 s0, -1
	s_lshl_b32 s4, s48, 8
	v_mbcnt_lo_u32_b32 v128, s0, 0
	v_mbcnt_hi_u32_b32 v146, s0, v128
	s_lshl_b32 s0, s42, 8
	v_lshrrev_b32_e32 v252, 4, v146
	s_or_b32 s0, s0, s67
	v_lshl_add_u32 v186, v252, 3, s0
	s_ashr_i32 s0, s48, 31
	s_lshr_b32 s0, s0, 28
	s_add_i32 s0, s48, s0
	s_ashr_i32 s0, s0, 4
	s_add_i32 s4, s4, s66
	s_ashr_i32 s1, s0, 31
	s_mul_i32 s39, s0, 0xc000
	s_mul_hi_i32 s5, s0, 0xc000
	s_add_u32 s48, s31, s39
	s_addc_u32 s49, s62, s5
	s_lshl_b64 s[0:1], s[0:1], 13
	v_ashrrev_i32_e32 v187, 31, v186
	s_add_u32 s0, s63, s0
	v_lshlrev_b64 v[128:129], 2, v[186:187]
	s_addc_u32 s1, s64, s1
	v_lshl_add_u64 v[190:191], s[0:1], 0, v[128:129]
	s_ashr_i32 s0, s4, 4
	v_ashrrev_i32_e32 v144, 5, v186
	s_ashr_i32 s1, s0, 31
	v_and_b32_e32 v147, 15, v146
	v_ashrrev_i32_e32 v145, 31, v144
	v_and_b32_e32 v146, 48, v146
	s_lshl_b64 s[0:1], s[0:1], 6
	v_or_b32_e32 v250, s4, v147
	v_lshl_or_b32 v212, v147, 6, v146
	v_lshl_add_u64 v[146:147], s[0:1], 0, v[144:145]
	v_lshl_add_u64 v[184:185], s[22:23], 0, v[212:213]
	v_lshlrev_b64 v[206:207], 10, v[146:147]
	v_lshl_add_u64 v[188:189], s[48:49], 0, v[128:129]
	v_lshl_add_u64 v[146:147], v[184:185], 0, v[206:207]
	global_load_dwordx4 v[136:139], v[188:189], off offset:16
	global_load_dwordx4 v[140:143], v[188:189], off
	global_load_dwordx4 v[128:131], v[190:191], off offset:16
	global_load_dwordx4 v[132:135], v[190:191], off
	global_load_dwordx4 v[240:243], v[146:147], off
	v_or_b32_e32 v246, 16, v250
	v_ashrrev_i32_e32 v146, 4, v246
	v_ashrrev_i32_e32 v147, 31, v146
	v_lshlrev_b64 v[202:203], 6, v[146:147]
	v_lshl_add_u64 v[146:147], v[202:203], 0, v[144:145]
	v_lshlrev_b64 v[208:209], 10, v[146:147]
	v_lshl_add_u64 v[146:147], v[184:185], 0, v[208:209]
	global_load_dwordx4 v[168:171], v[146:147], off
	v_or_b32_e32 v247, 32, v250
	v_ashrrev_i32_e32 v146, 4, v247
	v_ashrrev_i32_e32 v147, 31, v146
	v_lshlrev_b64 v[192:193], 6, v[146:147]
	v_lshl_add_u64 v[146:147], v[192:193], 0, v[144:145]
	v_lshlrev_b64 v[210:211], 10, v[146:147]
	v_lshl_add_u64 v[146:147], v[184:185], 0, v[210:211]
	global_load_dwordx4 v[164:167], v[146:147], off
	v_or_b32_e32 v217, 48, v250
	v_ashrrev_i32_e32 v146, 4, v217
	v_ashrrev_i32_e32 v147, 31, v146
	v_lshlrev_b64 v[194:195], 6, v[146:147]
	v_lshl_add_u64 v[146:147], v[194:195], 0, v[144:145]
	v_lshlrev_b64 v[224:225], 10, v[146:147]
	v_lshl_add_u64 v[146:147], v[184:185], 0, v[224:225]
	global_load_dwordx4 v[160:163], v[146:147], off
	v_add_u32_e32 v216, 0x80, v250
	v_ashrrev_i32_e32 v146, 4, v216
	v_ashrrev_i32_e32 v147, 31, v146
	v_lshlrev_b64 v[196:197], 6, v[146:147]
	v_lshl_add_u64 v[146:147], v[196:197], 0, v[144:145]
	v_lshlrev_b64 v[226:227], 10, v[146:147]
	v_lshl_add_u64 v[146:147], v[184:185], 0, v[226:227]
	global_load_dwordx4 v[156:159], v[146:147], off
	v_add_u32_e32 v245, 0x90, v250
	v_ashrrev_i32_e32 v146, 4, v245
	v_ashrrev_i32_e32 v147, 31, v146
	v_lshlrev_b64 v[198:199], 6, v[146:147]
	v_lshl_add_u64 v[146:147], v[198:199], 0, v[144:145]
	v_lshlrev_b64 v[230:231], 10, v[146:147]
	v_lshl_add_u64 v[146:147], v[184:185], 0, v[230:231]
	v_add_u32_e32 v244, 0xa0, v250
	global_load_dwordx4 v[152:155], v[146:147], off
	v_ashrrev_i32_e32 v146, 4, v244
	v_ashrrev_i32_e32 v147, 31, v146
	v_lshlrev_b64 v[200:201], 6, v[146:147]
	v_lshl_add_u64 v[146:147], v[200:201], 0, v[144:145]
	v_lshlrev_b64 v[232:233], 10, v[146:147]
	v_lshl_add_u64 v[146:147], v[184:185], 0, v[232:233]
	v_add_u32_e32 v187, 0xb0, v250
	global_load_dwordx4 v[148:151], v[146:147], off
	v_ashrrev_i32_e32 v146, 4, v187
	v_ashrrev_i32_e32 v147, 31, v146
	v_lshlrev_b64 v[204:205], 6, v[146:147]
	v_lshl_add_u64 v[144:145], v[204:205], 0, v[144:145]
	v_lshlrev_b64 v[234:235], 10, v[144:145]
	v_lshl_add_u64 v[206:207], s[22:23], 0, v[206:207]
	v_lshl_add_u64 v[144:145], v[184:185], 0, v[234:235]
	v_lshl_add_u64 v[206:207], v[206:207], 0, v[212:213]
	global_load_dwordx4 v[144:147], v[144:145], off
	s_ashr_i32 s48, s4, 8
	v_ashrrev_i32_e32 v228, 6, v186
	s_ashr_i32 s49, s48, 31
	v_ashrrev_i32_e32 v229, 31, v228
	s_lshl_b64 s[48:49], s[48:49], 5
	v_bfe_u32 v239, v186, 5, 1
	v_cmp_eq_u32_e32 vcc, 2, v252
	s_waitcnt vmcnt(0)
	v_cvt_f32_f16_e32 v236, v240
	v_cvt_f32_f16_sdwa v237, v240 dst_sel:DWORD dst_unused:UNUSED_PAD src0_sel:WORD_1
	v_cvt_f32_f16_e32 v240, v241
	v_cvt_f32_f16_sdwa v241, v241 dst_sel:DWORD dst_unused:UNUSED_PAD src0_sel:WORD_1
	v_pk_fma_f32 v[124:125], v[124:125], v[140:141], v[236:237]
	v_cvt_f32_f16_e32 v236, v242
	v_pk_fma_f32 v[126:127], v[126:127], v[142:143], v[240:241]
	v_cvt_f32_f16_sdwa v237, v242 dst_sel:DWORD dst_unused:UNUSED_PAD src0_sel:WORD_1
	v_cvt_f32_f16_e32 v240, v243
	v_cvt_f32_f16_sdwa v241, v243 dst_sel:DWORD dst_unused:UNUSED_PAD src0_sel:WORD_1
	v_pk_fma_f32 v[236:237], v[120:121], v[136:137], v[236:237]
	v_cvt_pk_f16_f32 v120, v124, v125
	v_pk_fma_f32 v[240:241], v[122:123], v[138:139], v[240:241]
	v_cvt_pk_f16_f32 v121, v126, v127
	v_cvt_pk_f16_f32 v122, v236, v237
	v_cvt_pk_f16_f32 v123, v240, v241
	global_store_dwordx4 v[206:207], v[120:123], off nt
	v_mov_b32_e32 v207, v213
	s_nop 0
	v_mul_f32_e32 v120, v125, v125
	v_mul_f32_e32 v121, v127, v127
	v_fmac_f32_e32 v120, v124, v124
	v_fmac_f32_e32 v121, v126, v126
	v_add_f32_e32 v120, v120, v121
	v_mul_f32_e32 v121, v237, v237
	v_fmac_f32_e32 v121, v236, v236
	v_add_f32_e32 v120, v121, v120
	v_mul_f32_e32 v121, v241, v241
	v_fmac_f32_e32 v121, v240, v240
	v_add_f32_e32 v242, v121, v120
	v_pk_mul_f32 v[122:123], v[134:135], v[126:127]
	v_pk_mul_f32 v[120:121], v[132:133], v[124:125]
	v_pk_mul_f32 v[124:125], v[130:131], v[240:241]
	v_pk_mul_f32 v[126:127], v[128:129], v[236:237]
	v_cvt_pk_bf16_f32 v120, v120, v121
	v_cvt_pk_bf16_f32 v121, v122, v123
	s_nop 0
	v_cvt_pk_bf16_f32 v122, v126, v127
	v_cvt_pk_bf16_f32 v123, v124, v125
	v_lshl_add_u64 v[124:125], s[48:49], 0, v[228:229]
	v_or_b32_e32 v126, s76, v239
	v_lshlrev_b64 v[124:125], 15, v[124:125]
	v_lshl_add_u64 v[236:237], s[24:25], 0, v[124:125]
	v_lshl_or_b32 v206, v126, 10, v212
	v_lshl_add_u64 v[124:125], v[236:237], 0, v[206:207]
	global_store_dwordx4 v[124:125], v[120:123], off nt
	v_lshl_add_u64 v[124:125], s[22:23], 0, v[208:209]
	v_lshl_add_u64 v[124:125], v[124:125], 0, v[212:213]
	v_cvt_f32_f16_e32 v120, v168
	v_cvt_f32_f16_sdwa v121, v168 dst_sel:DWORD dst_unused:UNUSED_PAD src0_sel:WORD_1
	v_cvt_f32_f16_e32 v122, v169
	v_cvt_f32_f16_sdwa v123, v169 dst_sel:DWORD dst_unused:UNUSED_PAD src0_sel:WORD_1
	v_mov_b32_e32 v209, v213
	v_pk_fma_f32 v[116:117], v[116:117], v[140:141], v[120:121]
	v_cvt_f32_f16_e32 v120, v170
	v_pk_fma_f32 v[118:119], v[118:119], v[142:143], v[122:123]
	v_cvt_f32_f16_sdwa v121, v170 dst_sel:DWORD dst_unused:UNUSED_PAD src0_sel:WORD_1
	v_cvt_f32_f16_e32 v122, v171
	v_cvt_f32_f16_sdwa v123, v171 dst_sel:DWORD dst_unused:UNUSED_PAD src0_sel:WORD_1
	v_pk_fma_f32 v[112:113], v[112:113], v[136:137], v[120:121]
	v_cvt_pk_f16_f32 v120, v116, v117
	v_pk_fma_f32 v[114:115], v[114:115], v[138:139], v[122:123]
	v_cvt_pk_f16_f32 v121, v118, v119
	v_cvt_pk_f16_f32 v122, v112, v113
	v_cvt_pk_f16_f32 v123, v114, v115
	global_store_dwordx4 v[124:125], v[120:123], off nt
	v_pk_mul_f32 v[124:125], v[130:131], v[114:115]
	v_pk_mul_f32 v[126:127], v[128:129], v[112:113]
	v_pk_mul_f32 v[122:123], v[134:135], v[118:119]
	v_pk_mul_f32 v[120:121], v[132:133], v[116:117]
	s_nop 0
	v_cvt_pk_bf16_f32 v120, v120, v121
	v_cvt_pk_bf16_f32 v121, v122, v123
	v_cvt_pk_bf16_f32 v122, v126, v127
	v_cvt_pk_bf16_f32 v123, v124, v125
	v_lshrrev_b32_e32 v124, 3, v246
	v_and_or_b32 v124, v124, 26, v239
	v_lshl_or_b32 v208, v124, 10, v212
	v_lshl_add_u64 v[124:125], v[236:237], 0, v[208:209]
	global_store_dwordx4 v[124:125], v[120:123], off nt
	s_nop 1
	v_cvt_f32_f16_e32 v120, v164
	v_cvt_f32_f16_sdwa v121, v164 dst_sel:DWORD dst_unused:UNUSED_PAD src0_sel:WORD_1
	v_cvt_f32_f16_e32 v122, v165
	v_cvt_f32_f16_sdwa v123, v165 dst_sel:DWORD dst_unused:UNUSED_PAD src0_sel:WORD_1
	v_pk_fma_f32 v[108:109], v[108:109], v[140:141], v[120:121]
	v_cvt_f32_f16_e32 v120, v166
	v_pk_fma_f32 v[110:111], v[110:111], v[142:143], v[122:123]
	v_cvt_f32_f16_sdwa v121, v166 dst_sel:DWORD dst_unused:UNUSED_PAD src0_sel:WORD_1
	v_cvt_f32_f16_e32 v122, v167
	v_cvt_f32_f16_sdwa v123, v167 dst_sel:DWORD dst_unused:UNUSED_PAD src0_sel:WORD_1
	v_pk_fma_f32 v[120:121], v[104:105], v[136:137], v[120:121]
	v_lshl_add_u64 v[104:105], s[22:23], 0, v[210:211]
	v_pk_fma_f32 v[106:107], v[106:107], v[138:139], v[122:123]
	v_cvt_pk_f16_f32 v122, v108, v109
	v_cvt_pk_f16_f32 v123, v110, v111
	v_cvt_pk_f16_f32 v124, v120, v121
	v_cvt_pk_f16_f32 v125, v106, v107
	v_lshl_add_u64 v[104:105], v[104:105], 0, v[212:213]
	global_store_dwordx4 v[104:105], v[122:125], off nt
	v_pk_mul_f32 v[104:105], v[134:135], v[110:111]
	v_mov_b32_e32 v211, v213
	v_pk_mul_f32 v[122:123], v[132:133], v[108:109]
	v_pk_mul_f32 v[124:125], v[128:129], v[120:121]
	v_cvt_pk_bf16_f32 v122, v122, v123
	v_cvt_pk_bf16_f32 v123, v104, v105
	v_lshrrev_b32_e32 v104, 3, v247
	v_and_or_b32 v104, v104, 28, v239
	v_lshl_or_b32 v210, v104, 10, v212
	v_lshl_add_u64 v[104:105], v[236:237], 0, v[210:211]
	v_pk_mul_f32 v[126:127], v[130:131], v[106:107]
	v_cvt_pk_bf16_f32 v124, v124, v125
	s_nop 0
	v_cvt_pk_bf16_f32 v125, v126, v127
	global_store_dwordx4 v[104:105], v[122:125], off nt
	v_cvt_f32_f16_e32 v104, v161
	v_cvt_f32_f16_sdwa v105, v161 dst_sel:DWORD dst_unused:UNUSED_PAD src0_sel:WORD_1
	v_cvt_f32_f16_e32 v122, v160
	v_cvt_f32_f16_sdwa v123, v160 dst_sel:DWORD dst_unused:UNUSED_PAD src0_sel:WORD_1
	v_pk_fma_f32 v[104:105], v[102:103], v[142:143], v[104:105]
	v_cvt_f32_f16_e32 v102, v163
	v_pk_fma_f32 v[122:123], v[100:101], v[140:141], v[122:123]
	v_cvt_f32_f16_e32 v100, v162
	v_cvt_f32_f16_sdwa v101, v162 dst_sel:DWORD dst_unused:UNUSED_PAD src0_sel:WORD_1
	v_cvt_f32_f16_sdwa v103, v163 dst_sel:DWORD dst_unused:UNUSED_PAD src0_sel:WORD_1
	v_pk_fma_f32 v[126:127], v[96:97], v[136:137], v[100:101]
	v_pk_fma_f32 v[124:125], v[98:99], v[138:139], v[102:103]
	v_lshl_add_u64 v[100:101], s[22:23], 0, v[224:225]
	v_cvt_pk_f16_f32 v96, v122, v123
	v_cvt_pk_f16_f32 v97, v104, v105
	v_cvt_pk_f16_f32 v98, v126, v127
	v_cvt_pk_f16_f32 v99, v124, v125
	v_lshl_add_u64 v[100:101], v[100:101], 0, v[212:213]
	global_store_dwordx4 v[100:101], v[96:99], off nt
	v_pk_mul_f32 v[100:101], v[130:131], v[124:125]
	v_pk_mul_f32 v[102:103], v[128:129], v[126:127]
	v_pk_mul_f32 v[98:99], v[134:135], v[104:105]
	v_pk_mul_f32 v[96:97], v[132:133], v[122:123]
	v_mov_b32_e32 v225, v213
	v_cvt_pk_bf16_f32 v96, v96, v97
	v_cvt_pk_bf16_f32 v97, v98, v99
	v_cvt_pk_bf16_f32 v98, v102, v103
	v_cvt_pk_bf16_f32 v99, v100, v101
	v_lshrrev_b32_e32 v100, 3, v217
	v_and_or_b32 v100, v100, 30, v239
	v_lshl_or_b32 v224, v100, 10, v212
	v_lshl_add_u64 v[100:101], v[236:237], 0, v[224:225]
	global_store_dwordx4 v[100:101], v[96:99], off nt
	v_cvt_f32_f16_e32 v100, v157
	v_cvt_f32_f16_sdwa v101, v157 dst_sel:DWORD dst_unused:UNUSED_PAD src0_sel:WORD_1
	v_cvt_f32_f16_e32 v98, v156
	v_cvt_f32_f16_sdwa v99, v156 dst_sel:DWORD dst_unused:UNUSED_PAD src0_sel:WORD_1
	v_ashrrev_i32_e32 v96, 8, v216
	v_pk_fma_f32 v[156:157], v[94:95], v[142:143], v[100:101]
	v_cvt_f32_f16_e32 v94, v159
	v_pk_fma_f32 v[160:161], v[92:93], v[140:141], v[98:99]
	v_cvt_f32_f16_e32 v92, v158
	v_cvt_f32_f16_sdwa v93, v158 dst_sel:DWORD dst_unused:UNUSED_PAD src0_sel:WORD_1
	v_cvt_f32_f16_sdwa v95, v159 dst_sel:DWORD dst_unused:UNUSED_PAD src0_sel:WORD_1
	v_ashrrev_i32_e32 v97, 31, v96
	v_pk_fma_f32 v[162:163], v[88:89], v[136:137], v[92:93]
	v_pk_fma_f32 v[158:159], v[90:91], v[138:139], v[94:95]
	v_lshl_add_u64 v[92:93], s[22:23], 0, v[226:227]
	v_cvt_pk_f16_f32 v88, v160, v161
	v_cvt_pk_f16_f32 v89, v156, v157
	v_cvt_pk_f16_f32 v90, v162, v163
	v_cvt_pk_f16_f32 v91, v158, v159
	v_lshl_add_u64 v[92:93], v[92:93], 0, v[212:213]
	global_store_dwordx4 v[92:93], v[88:91], off nt
	v_pk_mul_f32 v[94:95], v[130:131], v[158:159]
	v_pk_mul_f32 v[92:93], v[128:129], v[162:163]
	v_pk_mul_f32 v[88:89], v[134:135], v[156:157]
	v_pk_mul_f32 v[90:91], v[132:133], v[160:161]
	v_lshlrev_b64 v[226:227], 5, v[96:97]
	v_cvt_pk_bf16_f32 v90, v90, v91
	v_cvt_pk_bf16_f32 v91, v88, v89
	v_cvt_pk_bf16_f32 v92, v92, v93
	v_cvt_pk_bf16_f32 v93, v94, v95
	v_lshl_add_u64 v[88:89], v[226:227], 0, v[228:229]
	v_lshrrev_b32_e32 v94, 3, v216
	v_and_or_b32 v94, v94, 24, v239
	v_lshlrev_b64 v[88:89], 15, v[88:89]
	v_lshl_add_u64 v[88:89], s[24:25], 0, v[88:89]
	v_lshl_or_b32 v228, v94, 10, v212
	v_mov_b32_e32 v229, v213
	v_lshl_add_u64 v[94:95], v[88:89], 0, v[228:229]
	global_store_dwordx4 v[94:95], v[90:93], off nt
	s_nop 1
	v_cvt_f32_f16_e32 v90, v152
	v_cvt_f32_f16_sdwa v91, v152 dst_sel:DWORD dst_unused:UNUSED_PAD src0_sel:WORD_1
	v_cvt_f32_f16_e32 v92, v153
	v_cvt_f32_f16_sdwa v93, v153 dst_sel:DWORD dst_unused:UNUSED_PAD src0_sel:WORD_1
	v_pk_fma_f32 v[164:165], v[84:85], v[140:141], v[90:91]
	v_cvt_f32_f16_e32 v84, v154
	v_pk_fma_f32 v[152:153], v[86:87], v[142:143], v[92:93]
	v_cvt_f32_f16_sdwa v85, v154 dst_sel:DWORD dst_unused:UNUSED_PAD src0_sel:WORD_1
	v_cvt_f32_f16_e32 v86, v155
	v_cvt_f32_f16_sdwa v87, v155 dst_sel:DWORD dst_unused:UNUSED_PAD src0_sel:WORD_1
	v_pk_fma_f32 v[166:167], v[80:81], v[136:137], v[84:85]
	v_lshl_add_u64 v[84:85], s[22:23], 0, v[230:231]
	v_pk_fma_f32 v[154:155], v[82:83], v[138:139], v[86:87]
	v_cvt_pk_f16_f32 v80, v164, v165
	v_cvt_pk_f16_f32 v81, v152, v153
	v_cvt_pk_f16_f32 v82, v166, v167
	v_cvt_pk_f16_f32 v83, v154, v155
	v_lshl_add_u64 v[84:85], v[84:85], 0, v[212:213]
	global_store_dwordx4 v[84:85], v[80:83], off nt
	v_pk_mul_f32 v[84:85], v[130:131], v[154:155]
	v_pk_mul_f32 v[86:87], v[128:129], v[166:167]
	v_pk_mul_f32 v[82:83], v[134:135], v[152:153]
	v_pk_mul_f32 v[80:81], v[132:133], v[164:165]
	v_mov_b32_e32 v231, v213
	v_cvt_pk_bf16_f32 v80, v80, v81
	v_cvt_pk_bf16_f32 v81, v82, v83
	v_cvt_pk_bf16_f32 v82, v86, v87
	v_cvt_pk_bf16_f32 v83, v84, v85
	v_lshrrev_b32_e32 v84, 3, v245
	v_and_or_b32 v84, v84, 26, v239
	v_lshl_or_b32 v230, v84, 10, v212
	v_lshl_add_u64 v[84:85], v[88:89], 0, v[230:231]
	global_store_dwordx4 v[84:85], v[80:83], off nt
	s_nop 1
	v_cvt_f32_f16_e32 v80, v148
	v_cvt_f32_f16_sdwa v81, v148 dst_sel:DWORD dst_unused:UNUSED_PAD src0_sel:WORD_1
	v_cvt_f32_f16_e32 v82, v149
	v_cvt_f32_f16_sdwa v83, v149 dst_sel:DWORD dst_unused:UNUSED_PAD src0_sel:WORD_1
	v_pk_fma_f32 v[168:169], v[76:77], v[140:141], v[80:81]
	v_cvt_f32_f16_e32 v76, v150
	v_pk_fma_f32 v[148:149], v[78:79], v[142:143], v[82:83]
	v_cvt_f32_f16_sdwa v77, v150 dst_sel:DWORD dst_unused:UNUSED_PAD src0_sel:WORD_1
	v_cvt_f32_f16_e32 v78, v151
	v_cvt_f32_f16_sdwa v79, v151 dst_sel:DWORD dst_unused:UNUSED_PAD src0_sel:WORD_1
	v_pk_fma_f32 v[170:171], v[72:73], v[136:137], v[76:77]
	v_lshl_add_u64 v[76:77], s[22:23], 0, v[232:233]
	v_pk_fma_f32 v[150:151], v[74:75], v[138:139], v[78:79]
	v_cvt_pk_f16_f32 v72, v168, v169
	v_cvt_pk_f16_f32 v73, v148, v149
	v_cvt_pk_f16_f32 v74, v170, v171
	v_cvt_pk_f16_f32 v75, v150, v151
	v_lshl_add_u64 v[76:77], v[76:77], 0, v[212:213]
	global_store_dwordx4 v[76:77], v[72:75], off nt
	v_pk_mul_f32 v[76:77], v[130:131], v[150:151]
	v_pk_mul_f32 v[78:79], v[128:129], v[170:171]
	v_pk_mul_f32 v[74:75], v[134:135], v[148:149]
	v_pk_mul_f32 v[72:73], v[132:133], v[168:169]
	v_mov_b32_e32 v233, v213
	v_cvt_pk_bf16_f32 v72, v72, v73
	v_cvt_pk_bf16_f32 v73, v74, v75
	v_cvt_pk_bf16_f32 v74, v78, v79
	v_cvt_pk_bf16_f32 v75, v76, v77
	v_lshrrev_b32_e32 v76, 3, v244
	v_and_or_b32 v76, v76, 28, v239
	v_lshl_or_b32 v232, v76, 10, v212
	v_lshl_add_u64 v[76:77], v[88:89], 0, v[232:233]
	global_store_dwordx4 v[76:77], v[72:75], off nt
	s_nop 1
	v_cvt_f32_f16_e32 v72, v144
	v_cvt_f32_f16_sdwa v73, v144 dst_sel:DWORD dst_unused:UNUSED_PAD src0_sel:WORD_1
	v_cvt_f32_f16_e32 v74, v145
	v_cvt_f32_f16_sdwa v75, v145 dst_sel:DWORD dst_unused:UNUSED_PAD src0_sel:WORD_1
	v_pk_fma_f32 v[140:141], v[68:69], v[140:141], v[72:73]
	v_cvt_f32_f16_e32 v68, v146
	v_pk_fma_f32 v[142:143], v[70:71], v[142:143], v[74:75]
	v_cvt_f32_f16_sdwa v69, v146 dst_sel:DWORD dst_unused:UNUSED_PAD src0_sel:WORD_1
	v_cvt_f32_f16_e32 v70, v147
	v_cvt_f32_f16_sdwa v71, v147 dst_sel:DWORD dst_unused:UNUSED_PAD src0_sel:WORD_1
	v_add_u32_e32 v146, 0x80, v186
	v_pk_fma_f32 v[136:137], v[64:65], v[136:137], v[68:69]
	v_lshl_add_u64 v[68:69], s[22:23], 0, v[234:235]
	v_pk_fma_f32 v[138:139], v[66:67], v[138:139], v[70:71]
	v_cvt_pk_f16_f32 v64, v140, v141
	v_cvt_pk_f16_f32 v65, v142, v143
	v_cvt_pk_f16_f32 v66, v136, v137
	v_cvt_pk_f16_f32 v67, v138, v139
	v_lshl_add_u64 v[68:69], v[68:69], 0, v[212:213]
	global_store_dwordx4 v[68:69], v[64:67], off nt
	v_pk_mul_f32 v[68:69], v[130:131], v[138:139]
	v_pk_mul_f32 v[70:71], v[128:129], v[136:137]
	v_pk_mul_f32 v[66:67], v[134:135], v[142:143]
	v_pk_mul_f32 v[64:65], v[132:133], v[140:141]
	v_mov_b32_e32 v129, v213
	v_cvt_pk_bf16_f32 v64, v64, v65
	v_cvt_pk_bf16_f32 v65, v66, v67
	v_cvt_pk_bf16_f32 v66, v70, v71
	v_cvt_pk_bf16_f32 v67, v68, v69
	v_lshrrev_b32_e32 v68, 3, v187
	v_and_or_b32 v68, v68, 30, v239
	v_lshl_or_b32 v128, v68, 10, v212
	v_lshl_add_u64 v[68:69], v[88:89], 0, v[128:129]
	v_ashrrev_i32_e32 v80, 5, v146
	global_store_dwordx4 v[68:69], v[64:67], off nt
	v_ashrrev_i32_e32 v81, 31, v80
	v_lshl_add_u64 v[82:83], s[0:1], 0, v[80:81]
	global_load_dwordx4 v[72:75], v[188:189], off offset:528
	global_load_dwordx4 v[76:79], v[188:189], off offset:512
	global_load_dwordx4 v[64:67], v[190:191], off offset:528
	global_load_dwordx4 v[68:71], v[190:191], off offset:512
	v_lshlrev_b64 v[190:191], 10, v[82:83]
	v_lshl_add_u64 v[82:83], v[184:185], 0, v[190:191]
	global_load_dwordx4 v[234:237], v[82:83], off
	v_lshl_add_u64 v[82:83], v[202:203], 0, v[80:81]
	v_lshlrev_b64 v[202:203], 10, v[82:83]
	v_lshl_add_u64 v[82:83], v[184:185], 0, v[202:203]
	global_load_dwordx4 v[244:247], v[82:83], off
	v_lshl_add_u64 v[82:83], v[192:193], 0, v[80:81]
	v_lshlrev_b64 v[188:189], 10, v[82:83]
	v_lshl_add_u64 v[82:83], v[184:185], 0, v[188:189]
	global_load_dwordx4 v[100:103], v[82:83], off
	v_lshl_add_u64 v[82:83], v[194:195], 0, v[80:81]
	v_lshlrev_b64 v[186:187], 10, v[82:83]
	v_lshl_add_u64 v[82:83], v[184:185], 0, v[186:187]
	global_load_dwordx4 v[96:99], v[82:83], off
	v_lshl_add_u64 v[82:83], v[196:197], 0, v[80:81]
	v_lshlrev_b64 v[144:145], 10, v[82:83]
	v_lshl_add_u64 v[82:83], v[184:185], 0, v[144:145]
	global_load_dwordx4 v[92:95], v[82:83], off
	v_lshl_add_u64 v[82:83], v[198:199], 0, v[80:81]
	v_lshlrev_b64 v[134:135], 10, v[82:83]
	v_lshl_add_u64 v[82:83], v[184:185], 0, v[134:135]
	global_load_dwordx4 v[88:91], v[82:83], off
	v_lshl_add_u64 v[82:83], v[200:201], 0, v[80:81]
	v_lshlrev_b64 v[132:133], 10, v[82:83]
	v_lshl_add_u64 v[82:83], v[184:185], 0, v[132:133]
	v_lshl_add_u64 v[80:81], v[204:205], 0, v[80:81]
	global_load_dwordx4 v[84:87], v[82:83], off
	v_lshlrev_b64 v[130:131], 10, v[80:81]
	v_lshl_add_u64 v[80:81], v[184:185], 0, v[130:131]
	v_lshl_add_u64 v[190:191], s[22:23], 0, v[190:191]
	v_lshl_add_u64 v[190:191], v[190:191], 0, v[212:213]
	global_load_dwordx4 v[80:83], v[80:81], off
	v_ashrrev_i32_e32 v146, 6, v146
	v_ashrrev_i32_e32 v147, 31, v146
	s_lshl_b32 s0, s42, 2
	s_or_b32 s0, s0, s65
	s_waitcnt vmcnt(7)
	v_cvt_f32_f16_e32 v184, v234
	v_cvt_f32_f16_sdwa v185, v234 dst_sel:DWORD dst_unused:UNUSED_PAD src0_sel:WORD_1
	v_cvt_f32_f16_e32 v192, v235
	v_cvt_f32_f16_sdwa v193, v235 dst_sel:DWORD dst_unused:UNUSED_PAD src0_sel:WORD_1
	v_pk_fma_f32 v[60:61], v[60:61], v[76:77], v[184:185]
	v_cvt_f32_f16_e32 v184, v236
	v_pk_fma_f32 v[62:63], v[62:63], v[78:79], v[192:193]
	v_cvt_f32_f16_sdwa v185, v236 dst_sel:DWORD dst_unused:UNUSED_PAD src0_sel:WORD_1
	v_cvt_f32_f16_e32 v192, v237
	v_cvt_f32_f16_sdwa v193, v237 dst_sel:DWORD dst_unused:UNUSED_PAD src0_sel:WORD_1
	v_pk_fma_f32 v[184:185], v[56:57], v[72:73], v[184:185]
	v_cvt_pk_f16_f32 v56, v60, v61
	v_pk_fma_f32 v[192:193], v[58:59], v[74:75], v[192:193]
	v_cvt_pk_f16_f32 v57, v62, v63
	v_cvt_pk_f16_f32 v58, v184, v185
	v_cvt_pk_f16_f32 v59, v192, v193
	global_store_dwordx4 v[190:191], v[56:59], off nt
	v_pk_mul_f32 v[190:191], v[66:67], v[192:193]
	s_nop 0
	v_mul_f32_e32 v57, v63, v63
	v_fmac_f32_e32 v57, v62, v62
	v_pk_mul_f32 v[62:63], v[70:71], v[62:63]
	v_pk_mul_f32 v[58:59], v[68:69], v[60:61]
	v_mul_f32_e32 v56, v61, v61
	v_cvt_pk_bf16_f32 v58, v58, v59
	v_cvt_pk_bf16_f32 v59, v62, v63
	v_lshl_add_u64 v[62:63], s[48:49], 0, v[146:147]
	v_fmac_f32_e32 v56, v60, v60
	v_lshlrev_b64 v[62:63], 15, v[62:63]
	v_add_f32_e32 v56, v56, v57
	v_mul_f32_e32 v57, v185, v185
	v_pk_mul_f32 v[60:61], v[64:65], v[184:185]
	v_lshl_add_u64 v[62:63], s[24:25], 0, v[62:63]
	v_fmac_f32_e32 v57, v184, v184
	v_cvt_pk_bf16_f32 v60, v60, v61
	v_cvt_pk_bf16_f32 v61, v190, v191
	v_lshl_add_u64 v[184:185], v[62:63], 0, v[206:207]
	global_store_dwordx4 v[184:185], v[58:61], off nt
	v_lshl_add_u64 v[184:185], s[22:23], 0, v[202:203]
	v_lshl_add_u64 v[184:185], v[184:185], 0, v[212:213]
	s_waitcnt vmcnt(8)
	v_cvt_f32_f16_e32 v58, v244
	v_cvt_f32_f16_sdwa v59, v244 dst_sel:DWORD dst_unused:UNUSED_PAD src0_sel:WORD_1
	v_cvt_f32_f16_e32 v60, v245
	v_cvt_f32_f16_sdwa v61, v245 dst_sel:DWORD dst_unused:UNUSED_PAD src0_sel:WORD_1
	v_add_f32_e32 v56, v57, v56
	v_pk_fma_f32 v[52:53], v[52:53], v[76:77], v[58:59]
	v_cvt_f32_f16_e32 v58, v246
	v_pk_fma_f32 v[54:55], v[54:55], v[78:79], v[60:61]
	v_cvt_f32_f16_sdwa v59, v246 dst_sel:DWORD dst_unused:UNUSED_PAD src0_sel:WORD_1
	v_cvt_f32_f16_e32 v60, v247
	v_cvt_f32_f16_sdwa v61, v247 dst_sel:DWORD dst_unused:UNUSED_PAD src0_sel:WORD_1
	v_mul_f32_e32 v57, v193, v193
	v_pk_fma_f32 v[48:49], v[48:49], v[72:73], v[58:59]
	v_cvt_pk_f16_f32 v58, v52, v53
	v_pk_fma_f32 v[50:51], v[50:51], v[74:75], v[60:61]
	v_cvt_pk_f16_f32 v59, v54, v55
	v_cvt_pk_f16_f32 v60, v48, v49
	v_cvt_pk_f16_f32 v61, v50, v51
	global_store_dwordx4 v[184:185], v[58:61], off nt
	v_pk_mul_f32 v[184:185], v[66:67], v[50:51]
	v_pk_mul_f32 v[190:191], v[64:65], v[48:49]
	v_pk_mul_f32 v[60:61], v[70:71], v[54:55]
	v_pk_mul_f32 v[58:59], v[68:69], v[52:53]
	v_fmac_f32_e32 v57, v192, v192
	v_cvt_pk_bf16_f32 v58, v58, v59
	v_cvt_pk_bf16_f32 v59, v60, v61
	v_cvt_pk_bf16_f32 v60, v190, v191
	v_cvt_pk_bf16_f32 v61, v184, v185
	v_lshl_add_u64 v[184:185], v[62:63], 0, v[208:209]
	global_store_dwordx4 v[184:185], v[58:61], off nt
	v_add_f32_e32 v56, v57, v56
	v_add_f32_e32 v56, v242, v56
	s_waitcnt vmcnt(9)
	v_cvt_f32_f16_e32 v58, v100
	v_cvt_f32_f16_sdwa v59, v100 dst_sel:DWORD dst_unused:UNUSED_PAD src0_sel:WORD_1
	v_cvt_f32_f16_e32 v60, v101
	v_cvt_f32_f16_sdwa v61, v101 dst_sel:DWORD dst_unused:UNUSED_PAD src0_sel:WORD_1
	v_lshl_add_u64 v[100:101], s[22:23], 0, v[188:189]
	v_pk_fma_f32 v[44:45], v[44:45], v[76:77], v[58:59]
	v_cvt_f32_f16_e32 v58, v102
	v_pk_fma_f32 v[46:47], v[46:47], v[78:79], v[60:61]
	v_cvt_f32_f16_sdwa v59, v102 dst_sel:DWORD dst_unused:UNUSED_PAD src0_sel:WORD_1
	v_cvt_f32_f16_e32 v60, v103
	v_cvt_f32_f16_sdwa v61, v103 dst_sel:DWORD dst_unused:UNUSED_PAD src0_sel:WORD_1
	v_lshl_add_u64 v[100:101], v[100:101], 0, v[212:213]
	v_pk_fma_f32 v[40:41], v[40:41], v[72:73], v[58:59]
	v_cvt_pk_f16_f32 v58, v44, v45
	v_pk_fma_f32 v[42:43], v[42:43], v[74:75], v[60:61]
	v_cvt_pk_f16_f32 v59, v46, v47
	v_cvt_pk_f16_f32 v60, v40, v41
	v_cvt_pk_f16_f32 v61, v42, v43
	global_store_dwordx4 v[100:101], v[58:61], off nt
	v_pk_mul_f32 v[100:101], v[66:67], v[42:43]
	v_pk_mul_f32 v[102:103], v[64:65], v[40:41]
	v_pk_mul_f32 v[60:61], v[70:71], v[46:47]
	v_pk_mul_f32 v[58:59], v[68:69], v[44:45]
	ds_swizzle_b32 v57, v56 offset:swizzle(SWAP,16)
	v_cvt_pk_bf16_f32 v58, v58, v59
	v_cvt_pk_bf16_f32 v59, v60, v61
	v_cvt_pk_bf16_f32 v60, v102, v103
	v_cvt_pk_bf16_f32 v61, v100, v101
	v_lshl_add_u64 v[100:101], v[62:63], 0, v[210:211]
	global_store_dwordx4 v[100:101], v[58:61], off nt
	v_lshl_add_u64 v[62:63], v[62:63], 0, v[224:225]
	s_waitcnt lgkmcnt(0)
	v_add_f32_e32 v56, v56, v57
	s_waitcnt vmcnt(10)
	v_cvt_f32_f16_e32 v58, v96
	v_cvt_f32_f16_sdwa v59, v96 dst_sel:DWORD dst_unused:UNUSED_PAD src0_sel:WORD_1
	v_cvt_f32_f16_e32 v60, v97
	v_cvt_f32_f16_sdwa v61, v97 dst_sel:DWORD dst_unused:UNUSED_PAD src0_sel:WORD_1
	v_lshl_add_u64 v[96:97], s[22:23], 0, v[186:187]
	v_pk_fma_f32 v[36:37], v[36:37], v[76:77], v[58:59]
	v_cvt_f32_f16_e32 v58, v98
	v_pk_fma_f32 v[38:39], v[38:39], v[78:79], v[60:61]
	v_cvt_f32_f16_sdwa v59, v98 dst_sel:DWORD dst_unused:UNUSED_PAD src0_sel:WORD_1
	v_cvt_f32_f16_e32 v60, v99
	v_cvt_f32_f16_sdwa v61, v99 dst_sel:DWORD dst_unused:UNUSED_PAD src0_sel:WORD_1
	v_lshl_add_u64 v[96:97], v[96:97], 0, v[212:213]
	v_pk_fma_f32 v[32:33], v[32:33], v[72:73], v[58:59]
	v_cvt_pk_f16_f32 v58, v36, v37
	v_pk_fma_f32 v[34:35], v[34:35], v[74:75], v[60:61]
	v_cvt_pk_f16_f32 v59, v38, v39
	v_cvt_pk_f16_f32 v60, v32, v33
	v_cvt_pk_f16_f32 v61, v34, v35
	global_store_dwordx4 v[96:97], v[58:61], off nt
	v_pk_mul_f32 v[96:97], v[66:67], v[34:35]
	v_pk_mul_f32 v[98:99], v[64:65], v[32:33]
	v_pk_mul_f32 v[60:61], v[70:71], v[38:39]
	v_pk_mul_f32 v[58:59], v[68:69], v[36:37]
	v_mov_b32_e32 v57, v56
	v_cvt_pk_bf16_f32 v58, v58, v59
	v_cvt_pk_bf16_f32 v59, v60, v61
	v_cvt_pk_bf16_f32 v60, v98, v99
	v_cvt_pk_bf16_f32 v61, v96, v97
	global_store_dwordx4 v[62:63], v[58:61], off nt
	v_lshl_add_u64 v[62:63], s[22:23], 0, v[144:145]
	v_lshl_add_u64 v[62:63], v[62:63], 0, v[212:213]
	s_waitcnt vmcnt(11)
	v_cvt_f32_f16_e32 v58, v92
	v_cvt_f32_f16_sdwa v59, v92 dst_sel:DWORD dst_unused:UNUSED_PAD src0_sel:WORD_1
	v_cvt_f32_f16_e32 v60, v93
	v_cvt_f32_f16_sdwa v61, v93 dst_sel:DWORD dst_unused:UNUSED_PAD src0_sel:WORD_1
	v_pk_fma_f32 v[28:29], v[28:29], v[76:77], v[58:59]
	v_cvt_f32_f16_e32 v58, v94
	v_pk_fma_f32 v[30:31], v[30:31], v[78:79], v[60:61]
	v_cvt_f32_f16_sdwa v59, v94 dst_sel:DWORD dst_unused:UNUSED_PAD src0_sel:WORD_1
	v_cvt_f32_f16_e32 v60, v95
	v_cvt_f32_f16_sdwa v61, v95 dst_sel:DWORD dst_unused:UNUSED_PAD src0_sel:WORD_1
	v_pk_fma_f32 v[24:25], v[24:25], v[72:73], v[58:59]
	v_cvt_pk_f16_f32 v58, v28, v29
	v_pk_fma_f32 v[26:27], v[26:27], v[74:75], v[60:61]
	v_cvt_pk_f16_f32 v59, v30, v31
	v_cvt_pk_f16_f32 v60, v24, v25
	v_cvt_pk_f16_f32 v61, v26, v27
	global_store_dwordx4 v[62:63], v[58:61], off nt
	v_pk_mul_f32 v[62:63], v[66:67], v[26:27]
	v_pk_mul_f32 v[92:93], v[64:65], v[24:25]
	v_pk_mul_f32 v[60:61], v[70:71], v[30:31]
	v_pk_mul_f32 v[58:59], v[68:69], v[28:29]
	s_nop 0
	v_cvt_pk_bf16_f32 v58, v58, v59
	v_cvt_pk_bf16_f32 v59, v60, v61
	v_cvt_pk_bf16_f32 v60, v92, v93
	v_cvt_pk_bf16_f32 v61, v62, v63
	v_lshl_add_u64 v[62:63], v[226:227], 0, v[146:147]
	v_lshlrev_b64 v[62:63], 15, v[62:63]
	v_lshl_add_u64 v[62:63], s[24:25], 0, v[62:63]
	v_lshl_add_u64 v[92:93], v[62:63], 0, v[228:229]
	global_store_dwordx4 v[92:93], v[58:61], off nt
	s_waitcnt vmcnt(12)
	s_nop 0
	v_cvt_f32_f16_e32 v58, v88
	v_cvt_f32_f16_sdwa v59, v88 dst_sel:DWORD dst_unused:UNUSED_PAD src0_sel:WORD_1
	v_cvt_f32_f16_e32 v60, v89
	v_cvt_f32_f16_sdwa v61, v89 dst_sel:DWORD dst_unused:UNUSED_PAD src0_sel:WORD_1
	v_lshl_add_u64 v[88:89], s[22:23], 0, v[134:135]
	v_pk_fma_f32 v[20:21], v[20:21], v[76:77], v[58:59]
	v_cvt_f32_f16_e32 v58, v90
	v_pk_fma_f32 v[22:23], v[22:23], v[78:79], v[60:61]
	v_cvt_f32_f16_sdwa v59, v90 dst_sel:DWORD dst_unused:UNUSED_PAD src0_sel:WORD_1
	v_cvt_f32_f16_e32 v60, v91
	v_cvt_f32_f16_sdwa v61, v91 dst_sel:DWORD dst_unused:UNUSED_PAD src0_sel:WORD_1
	v_lshl_add_u64 v[88:89], v[88:89], 0, v[212:213]
	v_pk_fma_f32 v[16:17], v[16:17], v[72:73], v[58:59]
	v_cvt_pk_f16_f32 v58, v20, v21
	v_pk_fma_f32 v[18:19], v[18:19], v[74:75], v[60:61]
	v_cvt_pk_f16_f32 v59, v22, v23
	v_cvt_pk_f16_f32 v60, v16, v17
	v_cvt_pk_f16_f32 v61, v18, v19
	global_store_dwordx4 v[88:89], v[58:61], off nt
	v_pk_mul_f32 v[88:89], v[66:67], v[18:19]
	v_pk_mul_f32 v[90:91], v[64:65], v[16:17]
	v_pk_mul_f32 v[60:61], v[70:71], v[22:23]
	v_pk_mul_f32 v[58:59], v[68:69], v[20:21]
	s_nop 0
	v_cvt_pk_bf16_f32 v58, v58, v59
	v_cvt_pk_bf16_f32 v59, v60, v61
	v_cvt_pk_bf16_f32 v60, v90, v91
	v_cvt_pk_bf16_f32 v61, v88, v89
	v_lshl_add_u64 v[88:89], v[62:63], 0, v[230:231]
	global_store_dwordx4 v[88:89], v[58:61], off nt
	s_waitcnt vmcnt(13)
	s_nop 0
	v_cvt_f32_f16_e32 v58, v84
	v_cvt_f32_f16_sdwa v59, v84 dst_sel:DWORD dst_unused:UNUSED_PAD src0_sel:WORD_1
	v_cvt_f32_f16_e32 v60, v85
	v_cvt_f32_f16_sdwa v61, v85 dst_sel:DWORD dst_unused:UNUSED_PAD src0_sel:WORD_1
	v_lshl_add_u64 v[84:85], s[22:23], 0, v[132:133]
	v_pk_fma_f32 v[12:13], v[12:13], v[76:77], v[58:59]
	v_cvt_f32_f16_e32 v58, v86
	v_pk_fma_f32 v[14:15], v[14:15], v[78:79], v[60:61]
	v_cvt_f32_f16_sdwa v59, v86 dst_sel:DWORD dst_unused:UNUSED_PAD src0_sel:WORD_1
	v_cvt_f32_f16_e32 v60, v87
	v_cvt_f32_f16_sdwa v61, v87 dst_sel:DWORD dst_unused:UNUSED_PAD src0_sel:WORD_1
	v_lshl_add_u64 v[84:85], v[84:85], 0, v[212:213]
	v_pk_fma_f32 v[8:9], v[8:9], v[72:73], v[58:59]
	v_cvt_pk_f16_f32 v58, v12, v13
	v_pk_fma_f32 v[10:11], v[10:11], v[74:75], v[60:61]
	v_cvt_pk_f16_f32 v59, v14, v15
	v_cvt_pk_f16_f32 v60, v8, v9
	v_cvt_pk_f16_f32 v61, v10, v11
	global_store_dwordx4 v[84:85], v[58:61], off nt
	v_pk_mul_f32 v[84:85], v[66:67], v[10:11]
	v_pk_mul_f32 v[86:87], v[64:65], v[8:9]
	v_pk_mul_f32 v[60:61], v[70:71], v[14:15]
	v_pk_mul_f32 v[58:59], v[68:69], v[12:13]
	s_nop 0
	v_cvt_pk_bf16_f32 v58, v58, v59
	v_cvt_pk_bf16_f32 v59, v60, v61
	v_cvt_pk_bf16_f32 v60, v86, v87
	v_cvt_pk_bf16_f32 v61, v84, v85
	v_lshl_add_u64 v[84:85], v[62:63], 0, v[232:233]
	global_store_dwordx4 v[84:85], v[58:61], off nt
	v_lshl_add_u64 v[62:63], v[62:63], 0, v[128:129]
	s_waitcnt vmcnt(14)
	v_cvt_f32_f16_e32 v58, v80
	v_cvt_f32_f16_sdwa v59, v80 dst_sel:DWORD dst_unused:UNUSED_PAD src0_sel:WORD_1
	v_cvt_f32_f16_e32 v60, v81
	v_cvt_f32_f16_sdwa v61, v81 dst_sel:DWORD dst_unused:UNUSED_PAD src0_sel:WORD_1
	v_pk_fma_f32 v[4:5], v[4:5], v[76:77], v[58:59]
	v_cvt_f32_f16_e32 v58, v82
	v_pk_fma_f32 v[6:7], v[6:7], v[78:79], v[60:61]
	v_cvt_f32_f16_sdwa v59, v82 dst_sel:DWORD dst_unused:UNUSED_PAD src0_sel:WORD_1
	v_cvt_f32_f16_e32 v60, v83
	v_cvt_f32_f16_sdwa v61, v83 dst_sel:DWORD dst_unused:UNUSED_PAD src0_sel:WORD_1
	v_pk_fma_f32 v[0:1], v[0:1], v[72:73], v[58:59]
	v_lshl_add_u64 v[72:73], s[22:23], 0, v[130:131]
	v_pk_fma_f32 v[2:3], v[2:3], v[74:75], v[60:61]
	v_cvt_pk_f16_f32 v58, v4, v5
	v_cvt_pk_f16_f32 v59, v6, v7
	v_cvt_pk_f16_f32 v60, v0, v1
	v_cvt_pk_f16_f32 v61, v2, v3
	v_lshl_add_u64 v[72:73], v[72:73], 0, v[212:213]
	global_store_dwordx4 v[72:73], v[58:61], off nt
	v_pk_mul_f32 v[66:67], v[66:67], v[2:3]
	v_pk_mul_f32 v[64:65], v[64:65], v[0:1]
	v_pk_mul_f32 v[60:61], v[70:71], v[6:7]
	v_pk_mul_f32 v[58:59], v[68:69], v[4:5]
	v_lshl_add_u32 v212, v250, 5, s0
	v_cvt_pk_bf16_f32 v58, v58, v59
	v_cvt_pk_bf16_f32 v59, v60, v61
	v_cvt_pk_bf16_f32 v60, v64, v65
	v_cvt_pk_bf16_f32 v61, v66, v67
	global_store_dwordx4 v[62:63], v[58:61], off nt
	s_nop 1
	v_mov_b32_e32 v58, v56
	s_nop 1
	v_permlane32_swap_b32_e32 v57, v58
	s_and_saveexec_b64 s[0:1], vcc
	s_cbranch_execz .LBB0_1060
	v_add_f32_e32 v58, v56, v57
	v_lshl_add_u64 v[56:57], v[212:213], 2, s[20:21]
	global_store_dword v[56:57], v58, off

.LBB0_1176:
	s_mov_b32 s0, -1
	s_lshl_b32 s1, s75, 10
	v_mbcnt_lo_u32_b32 v108, s0, 0
	v_mbcnt_hi_u32_b32 v108, s0, v108
	v_lshrrev_b32_e32 v162, 1, v108
	v_and_b32_e32 v158, 56, v162
	s_add_i32 s4, s71, s1
	v_and_b32_e32 v161, 15, v108
	v_lshl_add_u32 v108, v158, 2, s4
	s_lshl_b32 s4, s74, 8
	s_lshl_b32 s0, s44, 8
	s_add_i32 s1, s72, s1
	s_or_b32 s4, s4, s61
	s_add_i32 s0, s0, s60
	v_add_u32_e32 v163, s4, v158
	v_lshl_add_u32 v158, v161, 2, s1
	v_and_b32_e32 v162, 24, v162
	v_or_b32_e32 v160, s0, v161
	ds_read_b128 v[124:127], v108
	ds_read_b128 v[120:123], v108 offset:16
	ds_read_b128 v[112:115], v108 offset:512
	ds_read_b128 v[108:111], v108 offset:528
	v_lshl_or_b32 v161, v161, 5, v162
	ds_read_b32 v162, v158
	s_ashr_i32 s0, s0, 8
	s_ashr_i32 s1, s0, 31
	s_lshl_b64 s[0:1], s[0:1], 7
	v_bfe_u32 v159, v163, 5, 1
	s_waitcnt lgkmcnt(0)
	v_pk_fma_f32 v[142:143], v[142:143], v[162:163], v[126:127] op_sel_hi:[1,0,1]
	v_pk_fma_f32 v[140:141], v[140:141], v[162:163], v[124:125] op_sel_hi:[1,0,1]
	v_pk_fma_f32 v[136:137], v[136:137], v[162:163], v[120:121] op_sel_hi:[1,0,1]
	v_max_f32_e32 v141, 0, v141
	v_max_f32_e32 v140, 0, v140
	v_max_f32_e32 v143, 0, v143
	v_max_f32_e32 v142, 0, v142
	v_max_f32_e32 v137, 0, v137
	v_max_f32_e32 v136, 0, v136
	v_pk_fma_f32 v[138:139], v[138:139], v[162:163], v[122:123] op_sel_hi:[1,0,1]
	v_pk_mul_f32 v[142:143], v[142:143], v[142:143]
	v_pk_mul_f32 v[140:141], v[140:141], v[140:141]
	v_pk_mul_f32 v[136:137], v[136:137], v[136:137]
	v_max_f32_e32 v139, 0, v139
	v_max_f32_e32 v138, 0, v138
	v_cvt_pk_bf16_f32 v140, v140, v141
	v_cvt_pk_bf16_f32 v141, v142, v143
	v_cvt_pk_bf16_f32 v142, v136, v137
	v_ashrrev_i32_e32 v136, 6, v163
	v_pk_mul_f32 v[138:139], v[138:139], v[138:139]
	v_ashrrev_i32_e32 v137, 31, v136
	v_cvt_pk_bf16_f32 v143, v138, v139
	v_lshl_add_u64 v[138:139], s[0:1], 0, v[136:137]
	v_or_b32_e32 v164, s70, v159
	v_lshlrev_b64 v[138:139], 15, v[138:139]
	v_lshlrev_b32_e32 v161, 1, v161
	v_pk_fma_f32 v[134:135], v[134:135], v[162:163], v[114:115] op_sel_hi:[1,0,1]
	v_pk_fma_f32 v[132:133], v[132:133], v[162:163], v[112:113] op_sel_hi:[1,0,1]
	v_pk_fma_f32 v[128:129], v[128:129], v[162:163], v[108:109] op_sel_hi:[1,0,1]
	v_lshl_add_u64 v[138:139], s[22:23], 0, v[138:139]
	v_lshl_or_b32 v212, v164, 10, v161
	v_max_f32_e32 v133, 0, v133
	v_max_f32_e32 v132, 0, v132
	v_max_f32_e32 v135, 0, v135
	v_max_f32_e32 v134, 0, v134
	v_max_f32_e32 v129, 0, v129
	v_max_f32_e32 v128, 0, v128
	v_lshl_add_u64 v[164:165], v[138:139], 0, v[212:213]
	v_pk_mul_f32 v[134:135], v[134:135], v[134:135]
	v_pk_mul_f32 v[132:133], v[132:133], v[132:133]
	v_pk_mul_f32 v[128:129], v[128:129], v[128:129]
	global_store_dwordx4 v[164:165], v[140:143], off nt
	v_pk_fma_f32 v[130:131], v[130:131], v[162:163], v[110:111] op_sel_hi:[1,0,1]
	v_cvt_pk_bf16_f32 v132, v132, v133
	v_cvt_pk_bf16_f32 v133, v134, v135
	v_cvt_pk_bf16_f32 v134, v128, v129
	v_add_u32_e32 v128, 0x80, v163
	v_max_f32_e32 v131, 0, v131
	v_max_f32_e32 v130, 0, v130
	v_ashrrev_i32_e32 v128, 6, v128
	v_pk_mul_f32 v[130:131], v[130:131], v[130:131]
	v_ashrrev_i32_e32 v129, 31, v128
	v_cvt_pk_bf16_f32 v135, v130, v131
	v_lshl_add_u64 v[130:131], s[0:1], 0, v[128:129]
	v_lshlrev_b64 v[130:131], 15, v[130:131]
	v_lshl_add_u64 v[130:131], s[22:23], 0, v[130:131]
	v_lshl_add_u64 v[140:141], v[130:131], 0, v[212:213]
	global_store_dwordx4 v[140:141], v[132:135], off nt
	ds_read_b32 v132, v158 offset:64
	s_mov_b64 s[0:1], -1
	s_andn2_b64 vcc, exec, s[36:37]
	s_waitcnt lgkmcnt(0)
	v_pk_fma_f32 v[118:119], v[118:119], v[132:133], v[126:127] op_sel_hi:[1,0,1]
	v_pk_fma_f32 v[116:117], v[116:117], v[132:133], v[124:125] op_sel_hi:[1,0,1]
	v_pk_fma_f32 v[106:107], v[106:107], v[132:133], v[122:123] op_sel_hi:[1,0,1]
	v_pk_fma_f32 v[104:105], v[104:105], v[132:133], v[120:121] op_sel_hi:[1,0,1]
	v_max_f32_e32 v117, 0, v117
	v_max_f32_e32 v116, 0, v116
	v_max_f32_e32 v119, 0, v119
	v_max_f32_e32 v118, 0, v118
	v_max_f32_e32 v105, 0, v105
	v_max_f32_e32 v104, 0, v104
	v_max_f32_e32 v107, 0, v107
	v_max_f32_e32 v106, 0, v106
	v_pk_fma_f32 v[100:101], v[100:101], v[132:133], v[112:113] op_sel_hi:[1,0,1]
	v_pk_fma_f32 v[98:99], v[98:99], v[132:133], v[110:111] op_sel_hi:[1,0,1]
	v_pk_fma_f32 v[96:97], v[96:97], v[132:133], v[108:109] op_sel_hi:[1,0,1]
	v_pk_mul_f32 v[118:119], v[118:119], v[118:119]
	v_pk_mul_f32 v[116:117], v[116:117], v[116:117]
	v_pk_mul_f32 v[134:135], v[106:107], v[106:107]
	v_pk_mul_f32 v[106:107], v[104:105], v[104:105]
	v_cvt_pk_bf16_f32 v104, v116, v117
	v_cvt_pk_bf16_f32 v105, v118, v119
	v_pk_fma_f32 v[102:103], v[102:103], v[132:133], v[114:115] op_sel_hi:[1,0,1]
	v_max_f32_e32 v101, 0, v101
	v_max_f32_e32 v100, 0, v100
	v_max_f32_e32 v97, 0, v97
	v_max_f32_e32 v96, 0, v96
	v_max_f32_e32 v99, 0, v99
	v_max_f32_e32 v98, 0, v98
	v_cvt_pk_bf16_f32 v106, v106, v107
	v_cvt_pk_bf16_f32 v107, v134, v135
	global_store_dwordx4 v[164:165], v[104:107], off offset:2048 nt
	v_max_f32_e32 v103, 0, v103
	v_max_f32_e32 v102, 0, v102
	v_pk_mul_f32 v[100:101], v[100:101], v[100:101]
	v_pk_mul_f32 v[104:105], v[98:99], v[98:99]
	v_pk_mul_f32 v[98:99], v[96:97], v[96:97]
	v_cvt_pk_bf16_f32 v96, v100, v101
	v_pk_mul_f32 v[102:103], v[102:103], v[102:103]
	s_nop 0
	v_cvt_pk_bf16_f32 v97, v102, v103
	v_cvt_pk_bf16_f32 v98, v98, v99
	v_cvt_pk_bf16_f32 v99, v104, v105
	global_store_dwordx4 v[140:141], v[96:99], off offset:2048 nt
	ds_read_b32 v96, v158 offset:128
	s_waitcnt lgkmcnt(0)
	v_pk_fma_f32 v[92:93], v[92:93], v[96:97], v[124:125] op_sel_hi:[1,0,1]
	v_pk_fma_f32 v[94:95], v[94:95], v[96:97], v[126:127] op_sel_hi:[1,0,1]
	v_pk_fma_f32 v[90:91], v[90:91], v[96:97], v[122:123] op_sel_hi:[1,0,1]
	v_pk_fma_f32 v[88:89], v[88:89], v[96:97], v[120:121] op_sel_hi:[1,0,1]
	v_max_f32_e32 v93, 0, v93
	v_max_f32_e32 v92, 0, v92
	v_max_f32_e32 v95, 0, v95
	v_max_f32_e32 v94, 0, v94
	v_max_f32_e32 v89, 0, v89
	v_max_f32_e32 v88, 0, v88
	v_max_f32_e32 v91, 0, v91
	v_max_f32_e32 v90, 0, v90
	v_pk_mul_f32 v[92:93], v[92:93], v[92:93]
	v_pk_fma_f32 v[84:85], v[84:85], v[96:97], v[112:113] op_sel_hi:[1,0,1]
	v_pk_mul_f32 v[94:95], v[94:95], v[94:95]
	v_pk_mul_f32 v[98:99], v[90:91], v[90:91]
	v_pk_mul_f32 v[90:91], v[88:89], v[88:89]
	v_cvt_pk_bf16_f32 v88, v92, v93
	v_or_b32_e32 v92, 0x1000, v212
	v_mov_b32_e32 v93, v213
	v_pk_fma_f32 v[82:83], v[82:83], v[96:97], v[110:111] op_sel_hi:[1,0,1]
	v_pk_fma_f32 v[80:81], v[80:81], v[96:97], v[108:109] op_sel_hi:[1,0,1]
	v_max_f32_e32 v85, 0, v85
	v_max_f32_e32 v84, 0, v84
	v_cvt_pk_bf16_f32 v89, v94, v95
	v_lshl_add_u64 v[94:95], v[138:139], 0, v[92:93]
	v_pk_fma_f32 v[86:87], v[86:87], v[96:97], v[114:115] op_sel_hi:[1,0,1]
	v_max_f32_e32 v81, 0, v81
	v_max_f32_e32 v80, 0, v80
	v_max_f32_e32 v83, 0, v83
	v_max_f32_e32 v82, 0, v82
	v_pk_mul_f32 v[84:85], v[84:85], v[84:85]
	v_cvt_pk_bf16_f32 v90, v90, v91
	v_cvt_pk_bf16_f32 v91, v98, v99
	global_store_dwordx4 v[94:95], v[88:91], off nt
	v_max_f32_e32 v87, 0, v87
	v_max_f32_e32 v86, 0, v86
	v_pk_mul_f32 v[88:89], v[82:83], v[82:83]
	v_pk_mul_f32 v[82:83], v[80:81], v[80:81]
	v_cvt_pk_bf16_f32 v80, v84, v85
	v_lshl_add_u64 v[84:85], v[130:131], 0, v[92:93]
	v_pk_mul_f32 v[86:87], v[86:87], v[86:87]
	v_or_b32_e32 v212, 0x1800, v212
	v_cvt_pk_bf16_f32 v81, v86, v87
	v_cvt_pk_bf16_f32 v82, v82, v83
	v_cvt_pk_bf16_f32 v83, v88, v89
	global_store_dwordx4 v[84:85], v[80:83], off nt
	ds_read_b32 v80, v158 offset:192
	s_waitcnt lgkmcnt(0)
	v_pk_fma_f32 v[76:77], v[76:77], v[80:81], v[124:125] op_sel_hi:[1,0,1]
	v_pk_fma_f32 v[78:79], v[78:79], v[80:81], v[126:127] op_sel_hi:[1,0,1]
	v_pk_fma_f32 v[74:75], v[74:75], v[80:81], v[122:123] op_sel_hi:[1,0,1]
	v_pk_fma_f32 v[72:73], v[72:73], v[80:81], v[120:121] op_sel_hi:[1,0,1]
	v_max_f32_e32 v77, 0, v77
	v_max_f32_e32 v76, 0, v76
	v_max_f32_e32 v79, 0, v79
	v_max_f32_e32 v78, 0, v78
	v_max_f32_e32 v73, 0, v73
	v_max_f32_e32 v72, 0, v72
	v_max_f32_e32 v75, 0, v75
	v_max_f32_e32 v74, 0, v74
	v_pk_mul_f32 v[76:77], v[76:77], v[76:77]
	v_pk_fma_f32 v[68:69], v[68:69], v[80:81], v[112:113] op_sel_hi:[1,0,1]
	v_pk_fma_f32 v[66:67], v[66:67], v[80:81], v[110:111] op_sel_hi:[1,0,1]
	v_pk_fma_f32 v[64:65], v[64:65], v[80:81], v[108:109] op_sel_hi:[1,0,1]
	v_pk_mul_f32 v[78:79], v[78:79], v[78:79]
	v_pk_mul_f32 v[82:83], v[74:75], v[74:75]
	v_pk_mul_f32 v[74:75], v[72:73], v[72:73]
	v_cvt_pk_bf16_f32 v72, v76, v77
	v_cvt_pk_bf16_f32 v73, v78, v79
	v_lshl_add_u64 v[76:77], v[138:139], 0, v[212:213]
	v_pk_fma_f32 v[70:71], v[70:71], v[80:81], v[114:115] op_sel_hi:[1,0,1]
	v_max_f32_e32 v69, 0, v69
	v_max_f32_e32 v68, 0, v68
	v_max_f32_e32 v65, 0, v65
	v_max_f32_e32 v64, 0, v64
	v_max_f32_e32 v67, 0, v67
	v_max_f32_e32 v66, 0, v66
	v_cvt_pk_bf16_f32 v74, v74, v75
	v_cvt_pk_bf16_f32 v75, v82, v83
	global_store_dwordx4 v[76:77], v[72:75], off nt
	v_max_f32_e32 v71, 0, v71
	v_max_f32_e32 v70, 0, v70
	v_pk_mul_f32 v[68:69], v[68:69], v[68:69]
	v_pk_mul_f32 v[72:73], v[66:67], v[66:67]
	v_pk_mul_f32 v[66:67], v[64:65], v[64:65]
	v_pk_mul_f32 v[70:71], v[70:71], v[70:71]
	v_cvt_pk_bf16_f32 v64, v68, v69
	v_lshl_add_u64 v[68:69], v[130:131], 0, v[212:213]
	v_cvt_pk_bf16_f32 v65, v70, v71
	v_cvt_pk_bf16_f32 v66, v66, v67
	v_cvt_pk_bf16_f32 v67, v72, v73
	global_store_dwordx4 v[68:69], v[64:67], off nt
	ds_read_b32 v66, v158 offset:512
	s_nop 0
	v_add_u32_e32 v67, 0x80, v160
	v_ashrrev_i32_e32 v64, 8, v67
	v_lshrrev_b32_e32 v67, 3, v67
	v_and_or_b32 v67, v67, 24, v159
	s_waitcnt lgkmcnt(0)
	v_pk_fma_f32 v[62:63], v[62:63], v[66:67], v[126:127] op_sel_hi:[1,0,1]
	v_pk_fma_f32 v[60:61], v[60:61], v[66:67], v[124:125] op_sel_hi:[1,0,1]
	v_pk_fma_f32 v[58:59], v[58:59], v[66:67], v[122:123] op_sel_hi:[1,0,1]
	v_pk_fma_f32 v[56:57], v[56:57], v[66:67], v[120:121] op_sel_hi:[1,0,1]
	v_max_f32_e32 v63, 0, v63
	v_max_f32_e32 v62, 0, v62
	v_ashrrev_i32_e32 v65, 31, v64
	v_max_f32_e32 v61, 0, v61
	v_max_f32_e32 v60, 0, v60
	v_max_f32_e32 v57, 0, v57
	v_max_f32_e32 v56, 0, v56
	v_max_f32_e32 v59, 0, v59
	v_max_f32_e32 v58, 0, v58
	v_pk_mul_f32 v[62:63], v[62:63], v[62:63]
	v_pk_mul_f32 v[60:61], v[60:61], v[60:61]
	v_pk_mul_f32 v[68:69], v[58:59], v[58:59]
	v_pk_mul_f32 v[56:57], v[56:57], v[56:57]
	v_cvt_pk_bf16_f32 v58, v60, v61
	v_cvt_pk_bf16_f32 v59, v62, v63
	v_lshlrev_b64 v[62:63], 7, v[64:65]
	v_cvt_pk_bf16_f32 v60, v56, v57
	v_lshl_add_u64 v[56:57], v[62:63], 0, v[136:137]
	v_lshlrev_b64 v[56:57], 15, v[56:57]
	v_pk_fma_f32 v[52:53], v[52:53], v[66:67], v[112:113] op_sel_hi:[1,0,1]
	v_pk_fma_f32 v[48:49], v[48:49], v[66:67], v[108:109] op_sel_hi:[1,0,1]
	v_lshl_add_u64 v[56:57], s[22:23], 0, v[56:57]
	v_lshl_or_b32 v212, v67, 10, v161
	v_pk_fma_f32 v[54:55], v[54:55], v[66:67], v[114:115] op_sel_hi:[1,0,1]
	v_pk_fma_f32 v[50:51], v[50:51], v[66:67], v[110:111] op_sel_hi:[1,0,1]
	v_max_f32_e32 v53, 0, v53
	v_max_f32_e32 v52, 0, v52
	v_max_f32_e32 v49, 0, v49
	v_max_f32_e32 v48, 0, v48
	v_lshl_add_u64 v[64:65], v[56:57], 0, v[212:213]
	v_max_f32_e32 v55, 0, v55
	v_max_f32_e32 v54, 0, v54
	v_max_f32_e32 v51, 0, v51
	v_max_f32_e32 v50, 0, v50
	v_pk_mul_f32 v[52:53], v[52:53], v[52:53]
	v_pk_mul_f32 v[48:49], v[48:49], v[48:49]
	v_cvt_pk_bf16_f32 v61, v68, v69
	global_store_dwordx4 v[64:65], v[58:61], off nt
	v_pk_mul_f32 v[54:55], v[54:55], v[54:55]
	s_nop 0
	v_pk_mul_f32 v[58:59], v[50:51], v[50:51]
	v_cvt_pk_bf16_f32 v50, v52, v53
	v_cvt_pk_bf16_f32 v51, v54, v55
	v_cvt_pk_bf16_f32 v52, v48, v49
	v_lshl_add_u64 v[48:49], v[62:63], 0, v[128:129]
	v_lshlrev_b64 v[48:49], 15, v[48:49]
	v_lshl_add_u64 v[48:49], s[22:23], 0, v[48:49]
	v_lshl_add_u64 v[54:55], v[48:49], 0, v[212:213]
	v_cvt_pk_bf16_f32 v53, v58, v59
	global_store_dwordx4 v[54:55], v[50:53], off nt
	ds_read_b32 v50, v158 offset:576
	s_waitcnt lgkmcnt(0)
	v_pk_fma_f32 v[46:47], v[46:47], v[50:51], v[126:127] op_sel_hi:[1,0,1]
	v_pk_fma_f32 v[44:45], v[44:45], v[50:51], v[124:125] op_sel_hi:[1,0,1]
	v_pk_fma_f32 v[42:43], v[42:43], v[50:51], v[122:123] op_sel_hi:[1,0,1]
	v_pk_fma_f32 v[40:41], v[40:41], v[50:51], v[120:121] op_sel_hi:[1,0,1]
	v_max_f32_e32 v45, 0, v45
	v_max_f32_e32 v44, 0, v44
	v_max_f32_e32 v47, 0, v47
	v_max_f32_e32 v46, 0, v46
	v_max_f32_e32 v41, 0, v41
	v_max_f32_e32 v40, 0, v40
	v_max_f32_e32 v43, 0, v43
	v_max_f32_e32 v42, 0, v42
	v_pk_fma_f32 v[36:37], v[36:37], v[50:51], v[112:113] op_sel_hi:[1,0,1]
	v_pk_fma_f32 v[34:35], v[34:35], v[50:51], v[110:111] op_sel_hi:[1,0,1]
	v_pk_fma_f32 v[32:33], v[32:33], v[50:51], v[108:109] op_sel_hi:[1,0,1]
	v_pk_mul_f32 v[46:47], v[46:47], v[46:47]
	v_pk_mul_f32 v[44:45], v[44:45], v[44:45]
	v_pk_mul_f32 v[52:53], v[42:43], v[42:43]
	v_pk_mul_f32 v[42:43], v[40:41], v[40:41]
	v_cvt_pk_bf16_f32 v40, v44, v45
	v_cvt_pk_bf16_f32 v41, v46, v47
	v_pk_fma_f32 v[38:39], v[38:39], v[50:51], v[114:115] op_sel_hi:[1,0,1]
	v_max_f32_e32 v37, 0, v37
	v_max_f32_e32 v36, 0, v36
	v_max_f32_e32 v33, 0, v33
	v_max_f32_e32 v32, 0, v32
	v_max_f32_e32 v35, 0, v35
	v_max_f32_e32 v34, 0, v34
	v_cvt_pk_bf16_f32 v42, v42, v43
	v_cvt_pk_bf16_f32 v43, v52, v53
	global_store_dwordx4 v[64:65], v[40:43], off offset:2048 nt
	v_max_f32_e32 v39, 0, v39
	v_max_f32_e32 v38, 0, v38
	v_pk_mul_f32 v[36:37], v[36:37], v[36:37]
	v_pk_mul_f32 v[40:41], v[34:35], v[34:35]
	v_pk_mul_f32 v[34:35], v[32:33], v[32:33]
	v_cvt_pk_bf16_f32 v32, v36, v37
	v_pk_mul_f32 v[38:39], v[38:39], v[38:39]
	s_nop 0
	v_cvt_pk_bf16_f32 v33, v38, v39
	v_cvt_pk_bf16_f32 v34, v34, v35
	v_cvt_pk_bf16_f32 v35, v40, v41
	global_store_dwordx4 v[54:55], v[32:35], off offset:2048 nt
	ds_read_b32 v32, v158 offset:640
	s_waitcnt lgkmcnt(0)
	v_pk_fma_f32 v[28:29], v[28:29], v[32:33], v[124:125] op_sel_hi:[1,0,1]
	v_pk_fma_f32 v[30:31], v[30:31], v[32:33], v[126:127] op_sel_hi:[1,0,1]
	v_pk_fma_f32 v[26:27], v[26:27], v[32:33], v[122:123] op_sel_hi:[1,0,1]
	v_pk_fma_f32 v[24:25], v[24:25], v[32:33], v[120:121] op_sel_hi:[1,0,1]
	v_max_f32_e32 v29, 0, v29
	v_max_f32_e32 v28, 0, v28
	v_max_f32_e32 v31, 0, v31
	v_max_f32_e32 v30, 0, v30
	v_max_f32_e32 v25, 0, v25
	v_max_f32_e32 v24, 0, v24
	v_max_f32_e32 v27, 0, v27
	v_max_f32_e32 v26, 0, v26
	v_pk_mul_f32 v[28:29], v[28:29], v[28:29]
	v_pk_fma_f32 v[20:21], v[20:21], v[32:33], v[112:113] op_sel_hi:[1,0,1]
	v_pk_mul_f32 v[30:31], v[30:31], v[30:31]
	v_pk_mul_f32 v[34:35], v[26:27], v[26:27]
	v_pk_mul_f32 v[26:27], v[24:25], v[24:25]
	v_cvt_pk_bf16_f32 v24, v28, v29
	v_or_b32_e32 v28, 0x1000, v212
	v_mov_b32_e32 v29, v213
	v_pk_fma_f32 v[18:19], v[18:19], v[32:33], v[110:111] op_sel_hi:[1,0,1]
	v_pk_fma_f32 v[16:17], v[16:17], v[32:33], v[108:109] op_sel_hi:[1,0,1]
	v_max_f32_e32 v21, 0, v21
	v_max_f32_e32 v20, 0, v20
	v_cvt_pk_bf16_f32 v25, v30, v31
	v_lshl_add_u64 v[30:31], v[56:57], 0, v[28:29]
	v_pk_fma_f32 v[22:23], v[22:23], v[32:33], v[114:115] op_sel_hi:[1,0,1]
	v_max_f32_e32 v17, 0, v17
	v_max_f32_e32 v16, 0, v16
	v_max_f32_e32 v19, 0, v19
	v_max_f32_e32 v18, 0, v18
	v_pk_mul_f32 v[20:21], v[20:21], v[20:21]
	v_cvt_pk_bf16_f32 v26, v26, v27
	v_cvt_pk_bf16_f32 v27, v34, v35
	global_store_dwordx4 v[30:31], v[24:27], off nt
	v_max_f32_e32 v23, 0, v23
	v_max_f32_e32 v22, 0, v22
	v_pk_mul_f32 v[24:25], v[18:19], v[18:19]
	v_pk_mul_f32 v[18:19], v[16:17], v[16:17]
	v_cvt_pk_bf16_f32 v16, v20, v21
	v_lshl_add_u64 v[20:21], v[48:49], 0, v[28:29]
	v_pk_mul_f32 v[22:23], v[22:23], v[22:23]
	v_or_b32_e32 v212, 0x1800, v212
	v_cvt_pk_bf16_f32 v17, v22, v23
	v_cvt_pk_bf16_f32 v18, v18, v19
	v_cvt_pk_bf16_f32 v19, v24, v25
	global_store_dwordx4 v[20:21], v[16:19], off nt
	ds_read_b32 v16, v158 offset:704
	s_waitcnt lgkmcnt(0)
	v_pk_fma_f32 v[12:13], v[12:13], v[16:17], v[124:125] op_sel_hi:[1,0,1]
	v_pk_fma_f32 v[14:15], v[14:15], v[16:17], v[126:127] op_sel_hi:[1,0,1]
	v_pk_fma_f32 v[10:11], v[10:11], v[16:17], v[122:123] op_sel_hi:[1,0,1]
	v_pk_fma_f32 v[8:9], v[8:9], v[16:17], v[120:121] op_sel_hi:[1,0,1]
	v_max_f32_e32 v13, 0, v13
	v_max_f32_e32 v12, 0, v12
	v_pk_fma_f32 v[4:5], v[4:5], v[16:17], v[112:113] op_sel_hi:[1,0,1]
	v_max_f32_e32 v15, 0, v15
	v_max_f32_e32 v14, 0, v14
	v_max_f32_e32 v9, 0, v9
	v_max_f32_e32 v8, 0, v8
	v_max_f32_e32 v11, 0, v11
	v_max_f32_e32 v10, 0, v10
	v_pk_mul_f32 v[12:13], v[12:13], v[12:13]
	v_pk_fma_f32 v[2:3], v[2:3], v[16:17], v[110:111] op_sel_hi:[1,0,1]
	v_pk_fma_f32 v[0:1], v[0:1], v[16:17], v[108:109] op_sel_hi:[1,0,1]
	v_max_f32_e32 v5, 0, v5
	v_max_f32_e32 v4, 0, v4
	v_pk_mul_f32 v[14:15], v[14:15], v[14:15]
	v_pk_mul_f32 v[18:19], v[10:11], v[10:11]
	v_pk_mul_f32 v[10:11], v[8:9], v[8:9]
	v_cvt_pk_bf16_f32 v8, v12, v13
	v_cvt_pk_bf16_f32 v9, v14, v15
	v_lshl_add_u64 v[12:13], v[56:57], 0, v[212:213]
	v_pk_fma_f32 v[6:7], v[6:7], v[16:17], v[114:115] op_sel_hi:[1,0,1]
	v_max_f32_e32 v1, 0, v1
	v_max_f32_e32 v0, 0, v0
	v_max_f32_e32 v3, 0, v3
	v_max_f32_e32 v2, 0, v2
	v_pk_mul_f32 v[4:5], v[4:5], v[4:5]
	v_cvt_pk_bf16_f32 v10, v10, v11
	v_cvt_pk_bf16_f32 v11, v18, v19
	global_store_dwordx4 v[12:13], v[8:11], off nt
	v_max_f32_e32 v7, 0, v7
	v_max_f32_e32 v6, 0, v6
	v_pk_mul_f32 v[8:9], v[2:3], v[2:3]
	v_pk_mul_f32 v[2:3], v[0:1], v[0:1]
	v_cvt_pk_bf16_f32 v0, v4, v5
	v_lshl_add_u64 v[4:5], v[48:49], 0, v[212:213]
	v_pk_mul_f32 v[6:7], v[6:7], v[6:7]
	s_nop 0
	v_cvt_pk_bf16_f32 v1, v6, v7
	v_cvt_pk_bf16_f32 v2, v2, v3
	v_cvt_pk_bf16_f32 v3, v8, v9
	global_store_dwordx4 v[4:5], v[0:3], off nt
	s_cbranch_vccnz .LBB0_1165
	s_andn2_b64 vcc, exec, s[20:21]
	s_cbranch_vccnz .LBB0_1164
	s_barrier
	s_branch .LBB0_1164

.LBB0_1251:
	s_mov_b32 s0, -1
	s_lshl_b32 s4, s42, 8
	v_mbcnt_lo_u32_b32 v72, s0, 0
	v_mbcnt_hi_u32_b32 v146, s0, v72
	s_lshl_b32 s0, s55, 8
	v_lshrrev_b32_e32 v147, 1, v146
	s_or_b32 s0, s0, s63
	v_and_b32_e32 v72, 56, v147
	v_add_u32_e32 v144, s0, v72
	s_ashr_i32 s0, s42, 31
	s_lshr_b32 s0, s0, 28
	s_add_i32 s0, s42, s0
	s_ashr_i32 s0, s0, 4
	s_add_i32 s4, s4, s62
	s_mul_hi_i32 s1, s0, 0xc000
	s_mul_i32 s0, s0, 0xc000
	s_add_u32 s0, s60, s0
	s_addc_u32 s1, s61, s1
	v_ashrrev_i32_e32 v145, 31, v144
	v_lshl_add_u64 v[76:77], v[144:145], 2, s[0:1]
	v_lshlrev_b32_e32 v145, 5, v146
	s_ashr_i32 s0, s4, 4
	v_and_b32_e32 v145, 0x1e0, v145
	v_ashrrev_i32_e32 v186, 5, v144
	s_ashr_i32 s1, s0, 31
	v_and_or_b32 v145, v147, 24, v145
	v_ashrrev_i32_e32 v187, 31, v186
	s_lshl_b64 s[44:45], s[0:1], 6
	v_lshlrev_b32_e32 v212, 1, v145
	v_lshl_add_u64 v[146:147], s[44:45], 0, v[186:187]
	v_lshl_add_u64 v[184:185], s[20:21], 0, v[212:213]
	v_lshlrev_b64 v[204:205], 10, v[146:147]
	v_lshl_add_u64 v[146:147], v[184:185], 0, v[204:205]
	global_load_dwordx4 v[84:87], v[76:77], off offset:16
	global_load_dwordx4 v[92:95], v[76:77], off
	global_load_dwordx4 v[72:75], v[76:77], off offset:528
	s_nop 0
	global_load_dwordx4 v[76:79], v[76:77], off offset:512
	v_add_u32_e32 v144, 0x80, v144
	global_load_dwordx4 v[208:211], v[146:147], off
	v_ashrrev_i32_e32 v188, 5, v144
	v_ashrrev_i32_e32 v189, 31, v188
	v_lshl_add_u64 v[144:145], s[44:45], 0, v[188:189]
	v_lshlrev_b64 v[202:203], 10, v[144:145]
	v_lshl_add_u64 v[144:145], v[184:185], 0, v[202:203]
	global_load_dwordx4 v[168:171], v[144:145], off
	s_or_b32 s44, s0, 1
	s_ashr_i32 s45, s44, 31
	s_lshl_b64 s[44:45], s[44:45], 6
	v_lshl_add_u64 v[144:145], s[44:45], 0, v[186:187]
	v_lshlrev_b64 v[200:201], 10, v[144:145]
	v_lshl_add_u64 v[144:145], v[184:185], 0, v[200:201]
	global_load_dwordx4 v[164:167], v[144:145], off
	v_lshl_add_u64 v[144:145], s[44:45], 0, v[188:189]
	v_lshlrev_b64 v[198:199], 10, v[144:145]
	v_lshl_add_u64 v[144:145], v[184:185], 0, v[198:199]
	global_load_dwordx4 v[160:163], v[144:145], off
	s_or_b32 s44, s0, 2
	s_ashr_i32 s45, s44, 31
	s_lshl_b64 s[44:45], s[44:45], 6
	v_lshl_add_u64 v[144:145], s[44:45], 0, v[186:187]
	v_lshlrev_b64 v[196:197], 10, v[144:145]
	v_lshl_add_u64 v[144:145], v[184:185], 0, v[196:197]
	global_load_dwordx4 v[156:159], v[144:145], off
	v_lshl_add_u64 v[144:145], s[44:45], 0, v[188:189]
	s_or_b32 s0, s0, 3
	v_lshlrev_b64 v[194:195], 10, v[144:145]
	s_ashr_i32 s1, s0, 31
	v_lshl_add_u64 v[144:145], v[184:185], 0, v[194:195]
	s_lshl_b64 s[0:1], s[0:1], 6
	global_load_dwordx4 v[152:155], v[144:145], off
	v_lshl_add_u64 v[144:145], s[0:1], 0, v[186:187]
	v_lshlrev_b64 v[192:193], 10, v[144:145]
	v_lshl_add_u64 v[144:145], v[184:185], 0, v[192:193]
	global_load_dwordx4 v[148:151], v[144:145], off
	v_lshl_add_u64 v[144:145], s[0:1], 0, v[188:189]
	v_lshlrev_b64 v[190:191], 10, v[144:145]
	v_lshl_add_u64 v[144:145], v[184:185], 0, v[190:191]
	global_load_dwordx4 v[144:147], v[144:145], off
	s_add_i32 s0, s4, 0x80
	s_ashr_i32 s0, s0, 4
	s_ashr_i32 s1, s0, 31
	s_lshl_b64 s[0:1], s[0:1], 6
	s_andn2_b64 vcc, exec, s[36:37]
	s_waitcnt vmcnt(0)
	v_cvt_f32_f16_e32 v224, v208
	v_cvt_f32_f16_sdwa v225, v208 dst_sel:DWORD dst_unused:UNUSED_PAD src0_sel:WORD_1
	v_cvt_f32_f16_e32 v208, v209
	v_cvt_f32_f16_sdwa v209, v209 dst_sel:DWORD dst_unused:UNUSED_PAD src0_sel:WORD_1
	v_pk_fma_f32 v[140:141], v[140:141], v[92:93], v[224:225]
	s_nop 0
	v_cvt_pk_f16_f32 v140, v140, v141
	v_pk_fma_f32 v[142:143], v[142:143], v[94:95], v[208:209]
	s_nop 0
	v_cvt_pk_f16_f32 v141, v142, v143
	v_cvt_f32_f16_e32 v142, v210
	v_cvt_f32_f16_sdwa v143, v210 dst_sel:DWORD dst_unused:UNUSED_PAD src0_sel:WORD_1
	v_pk_fma_f32 v[136:137], v[136:137], v[84:85], v[142:143]
	s_nop 0
	v_cvt_pk_f16_f32 v142, v136, v137
	v_cvt_f32_f16_e32 v136, v211
	v_cvt_f32_f16_sdwa v137, v211 dst_sel:DWORD dst_unused:UNUSED_PAD src0_sel:WORD_1
	v_pk_fma_f32 v[136:137], v[138:139], v[86:87], v[136:137]
	s_nop 0
	v_cvt_pk_f16_f32 v143, v136, v137
	v_lshl_add_u64 v[136:137], s[20:21], 0, v[204:205]
	v_lshl_add_u64 v[136:137], v[136:137], 0, v[212:213]
	global_store_dwordx4 v[136:137], v[140:143], off nt
	v_cvt_f32_f16_e32 v136, v168
	v_cvt_f32_f16_sdwa v137, v168 dst_sel:DWORD dst_unused:UNUSED_PAD src0_sel:WORD_1
	v_pk_fma_f32 v[132:133], v[132:133], v[76:77], v[136:137]
	v_cvt_f32_f16_e32 v136, v169
	v_cvt_f32_f16_sdwa v137, v169 dst_sel:DWORD dst_unused:UNUSED_PAD src0_sel:WORD_1
	v_cvt_pk_f16_f32 v132, v132, v133
	v_pk_fma_f32 v[134:135], v[134:135], v[78:79], v[136:137]
	s_nop 0
	v_cvt_pk_f16_f32 v133, v134, v135
	v_cvt_f32_f16_e32 v134, v170
	v_cvt_f32_f16_sdwa v135, v170 dst_sel:DWORD dst_unused:UNUSED_PAD src0_sel:WORD_1
	v_pk_fma_f32 v[128:129], v[128:129], v[72:73], v[134:135]
	s_nop 0
	v_cvt_pk_f16_f32 v134, v128, v129
	v_cvt_f32_f16_e32 v128, v171
	v_cvt_f32_f16_sdwa v129, v171 dst_sel:DWORD dst_unused:UNUSED_PAD src0_sel:WORD_1
	v_pk_fma_f32 v[128:129], v[130:131], v[74:75], v[128:129]
	s_nop 0
	v_cvt_pk_f16_f32 v135, v128, v129
	v_lshl_add_u64 v[128:129], s[20:21], 0, v[202:203]
	v_lshl_add_u64 v[128:129], v[128:129], 0, v[212:213]
	global_store_dwordx4 v[128:129], v[132:135], off nt
	v_cvt_f32_f16_e32 v128, v164
	v_cvt_f32_f16_sdwa v129, v164 dst_sel:DWORD dst_unused:UNUSED_PAD src0_sel:WORD_1
	v_pk_fma_f32 v[124:125], v[124:125], v[92:93], v[128:129]
	v_cvt_f32_f16_e32 v128, v165
	v_cvt_f32_f16_sdwa v129, v165 dst_sel:DWORD dst_unused:UNUSED_PAD src0_sel:WORD_1
	v_cvt_pk_f16_f32 v124, v124, v125
	v_pk_fma_f32 v[126:127], v[126:127], v[94:95], v[128:129]
	s_nop 0
	v_cvt_pk_f16_f32 v125, v126, v127
	v_cvt_f32_f16_e32 v126, v166
	v_cvt_f32_f16_sdwa v127, v166 dst_sel:DWORD dst_unused:UNUSED_PAD src0_sel:WORD_1
	v_pk_fma_f32 v[120:121], v[120:121], v[84:85], v[126:127]
	s_nop 0
	v_cvt_pk_f16_f32 v126, v120, v121
	v_cvt_f32_f16_e32 v120, v167
	v_cvt_f32_f16_sdwa v121, v167 dst_sel:DWORD dst_unused:UNUSED_PAD src0_sel:WORD_1
	v_pk_fma_f32 v[120:121], v[122:123], v[86:87], v[120:121]
	s_nop 0
	v_cvt_pk_f16_f32 v127, v120, v121
	v_lshl_add_u64 v[120:121], s[20:21], 0, v[200:201]
	v_lshl_add_u64 v[120:121], v[120:121], 0, v[212:213]
	global_store_dwordx4 v[120:121], v[124:127], off nt
	v_cvt_f32_f16_e32 v120, v160
	v_cvt_f32_f16_sdwa v121, v160 dst_sel:DWORD dst_unused:UNUSED_PAD src0_sel:WORD_1
	v_pk_fma_f32 v[116:117], v[116:117], v[76:77], v[120:121]
	v_cvt_f32_f16_e32 v120, v161
	v_cvt_f32_f16_sdwa v121, v161 dst_sel:DWORD dst_unused:UNUSED_PAD src0_sel:WORD_1
	v_cvt_pk_f16_f32 v116, v116, v117
	v_pk_fma_f32 v[118:119], v[118:119], v[78:79], v[120:121]
	s_nop 0
	v_cvt_pk_f16_f32 v117, v118, v119
	v_cvt_f32_f16_e32 v118, v162
	v_cvt_f32_f16_sdwa v119, v162 dst_sel:DWORD dst_unused:UNUSED_PAD src0_sel:WORD_1
	v_pk_fma_f32 v[112:113], v[112:113], v[72:73], v[118:119]
	s_nop 0
	v_cvt_pk_f16_f32 v118, v112, v113
	v_cvt_f32_f16_e32 v112, v163
	v_cvt_f32_f16_sdwa v113, v163 dst_sel:DWORD dst_unused:UNUSED_PAD src0_sel:WORD_1
	v_pk_fma_f32 v[112:113], v[114:115], v[74:75], v[112:113]
	s_nop 0
	v_cvt_pk_f16_f32 v119, v112, v113
	v_lshl_add_u64 v[112:113], s[20:21], 0, v[198:199]
	v_lshl_add_u64 v[112:113], v[112:113], 0, v[212:213]
	global_store_dwordx4 v[112:113], v[116:119], off nt
	v_cvt_f32_f16_e32 v112, v156
	v_cvt_f32_f16_sdwa v113, v156 dst_sel:DWORD dst_unused:UNUSED_PAD src0_sel:WORD_1
	v_pk_fma_f32 v[108:109], v[108:109], v[92:93], v[112:113]
	v_cvt_f32_f16_e32 v112, v157
	v_cvt_f32_f16_sdwa v113, v157 dst_sel:DWORD dst_unused:UNUSED_PAD src0_sel:WORD_1
	v_cvt_pk_f16_f32 v108, v108, v109
	v_pk_fma_f32 v[110:111], v[110:111], v[94:95], v[112:113]
	s_nop 0
	v_cvt_pk_f16_f32 v109, v110, v111
	v_cvt_f32_f16_e32 v110, v158
	v_cvt_f32_f16_sdwa v111, v158 dst_sel:DWORD dst_unused:UNUSED_PAD src0_sel:WORD_1
	v_pk_fma_f32 v[104:105], v[104:105], v[84:85], v[110:111]
	s_nop 0
	v_cvt_pk_f16_f32 v110, v104, v105
	v_cvt_f32_f16_e32 v104, v159
	v_cvt_f32_f16_sdwa v105, v159 dst_sel:DWORD dst_unused:UNUSED_PAD src0_sel:WORD_1
	v_pk_fma_f32 v[104:105], v[106:107], v[86:87], v[104:105]
	s_nop 0
	v_cvt_pk_f16_f32 v111, v104, v105
	v_lshl_add_u64 v[104:105], s[20:21], 0, v[196:197]
	v_lshl_add_u64 v[104:105], v[104:105], 0, v[212:213]
	global_store_dwordx4 v[104:105], v[108:111], off nt
	v_cvt_f32_f16_e32 v104, v152
	v_cvt_f32_f16_sdwa v105, v152 dst_sel:DWORD dst_unused:UNUSED_PAD src0_sel:WORD_1
	v_pk_fma_f32 v[100:101], v[100:101], v[76:77], v[104:105]
	v_cvt_f32_f16_e32 v104, v153
	v_cvt_f32_f16_sdwa v105, v153 dst_sel:DWORD dst_unused:UNUSED_PAD src0_sel:WORD_1
	v_cvt_pk_f16_f32 v100, v100, v101
	v_pk_fma_f32 v[102:103], v[102:103], v[78:79], v[104:105]
	s_nop 0
	v_cvt_pk_f16_f32 v101, v102, v103
	v_cvt_f32_f16_e32 v102, v154
	v_cvt_f32_f16_sdwa v103, v154 dst_sel:DWORD dst_unused:UNUSED_PAD src0_sel:WORD_1
	v_pk_fma_f32 v[96:97], v[96:97], v[72:73], v[102:103]
	s_nop 0
	v_cvt_pk_f16_f32 v102, v96, v97
	v_cvt_f32_f16_e32 v96, v155
	v_cvt_f32_f16_sdwa v97, v155 dst_sel:DWORD dst_unused:UNUSED_PAD src0_sel:WORD_1
	v_pk_fma_f32 v[96:97], v[98:99], v[74:75], v[96:97]
	s_nop 0
	v_cvt_pk_f16_f32 v103, v96, v97
	v_lshl_add_u64 v[96:97], s[20:21], 0, v[194:195]
	v_lshl_add_u64 v[96:97], v[96:97], 0, v[212:213]
	global_store_dwordx4 v[96:97], v[100:103], off nt
	v_cvt_f32_f16_e32 v96, v148
	v_cvt_f32_f16_sdwa v97, v148 dst_sel:DWORD dst_unused:UNUSED_PAD src0_sel:WORD_1
	v_pk_fma_f32 v[88:89], v[88:89], v[92:93], v[96:97]
	v_cvt_f32_f16_e32 v96, v149
	v_cvt_f32_f16_sdwa v97, v149 dst_sel:DWORD dst_unused:UNUSED_PAD src0_sel:WORD_1
	v_cvt_pk_f16_f32 v88, v88, v89
	v_pk_fma_f32 v[90:91], v[90:91], v[94:95], v[96:97]
	s_nop 0
	v_cvt_pk_f16_f32 v89, v90, v91
	v_cvt_f32_f16_e32 v90, v150
	v_cvt_f32_f16_sdwa v91, v150 dst_sel:DWORD dst_unused:UNUSED_PAD src0_sel:WORD_1
	v_pk_fma_f32 v[80:81], v[80:81], v[84:85], v[90:91]
	s_nop 0
	v_cvt_pk_f16_f32 v90, v80, v81
	v_cvt_f32_f16_e32 v80, v151
	v_cvt_f32_f16_sdwa v81, v151 dst_sel:DWORD dst_unused:UNUSED_PAD src0_sel:WORD_1
	v_pk_fma_f32 v[80:81], v[82:83], v[86:87], v[80:81]
	s_nop 0
	v_cvt_pk_f16_f32 v91, v80, v81
	v_lshl_add_u64 v[80:81], s[20:21], 0, v[192:193]
	v_lshl_add_u64 v[80:81], v[80:81], 0, v[212:213]
	global_store_dwordx4 v[80:81], v[88:91], off nt
	v_cvt_f32_f16_e32 v80, v144
	v_cvt_f32_f16_sdwa v81, v144 dst_sel:DWORD dst_unused:UNUSED_PAD src0_sel:WORD_1
	v_pk_fma_f32 v[68:69], v[68:69], v[76:77], v[80:81]
	v_cvt_f32_f16_e32 v80, v145
	v_cvt_f32_f16_sdwa v81, v145 dst_sel:DWORD dst_unused:UNUSED_PAD src0_sel:WORD_1
	v_cvt_pk_f16_f32 v68, v68, v69
	v_pk_fma_f32 v[70:71], v[70:71], v[78:79], v[80:81]
	s_nop 0
	v_cvt_pk_f16_f32 v69, v70, v71
	v_cvt_f32_f16_e32 v70, v146
	v_cvt_f32_f16_sdwa v71, v146 dst_sel:DWORD dst_unused:UNUSED_PAD src0_sel:WORD_1
	v_pk_fma_f32 v[64:65], v[64:65], v[72:73], v[70:71]
	s_nop 0
	v_cvt_pk_f16_f32 v70, v64, v65
	v_cvt_f32_f16_e32 v64, v147
	v_cvt_f32_f16_sdwa v65, v147 dst_sel:DWORD dst_unused:UNUSED_PAD src0_sel:WORD_1
	v_pk_fma_f32 v[64:65], v[66:67], v[74:75], v[64:65]
	s_nop 0
	v_cvt_pk_f16_f32 v71, v64, v65
	v_lshl_add_u64 v[64:65], s[20:21], 0, v[190:191]
	v_lshl_add_u64 v[64:65], v[64:65], 0, v[212:213]
	global_store_dwordx4 v[64:65], v[68:71], off nt
	v_lshl_add_u64 v[64:65], s[0:1], 0, v[186:187]
	v_lshlrev_b64 v[124:125], 10, v[64:65]
	v_lshl_add_u64 v[64:65], v[184:185], 0, v[124:125]
	global_load_dwordx4 v[116:119], v[64:65], off
	v_lshl_add_u64 v[64:65], s[0:1], 0, v[188:189]
	v_lshlrev_b64 v[126:127], 10, v[64:65]
	v_lshl_add_u64 v[64:65], v[184:185], 0, v[126:127]
	global_load_dwordx4 v[120:123], v[64:65], off
	s_add_i32 s0, s4, 0x90
	s_ashr_i32 s0, s0, 4
	s_ashr_i32 s1, s0, 31
	s_lshl_b64 s[0:1], s[0:1], 6
	v_lshl_add_u64 v[64:65], s[0:1], 0, v[186:187]
	v_lshlrev_b64 v[114:115], 10, v[64:65]
	v_lshl_add_u64 v[64:65], v[184:185], 0, v[114:115]
	global_load_dwordx4 v[100:103], v[64:65], off
	v_lshl_add_u64 v[64:65], s[0:1], 0, v[188:189]
	v_lshlrev_b64 v[112:113], 10, v[64:65]
	v_lshl_add_u64 v[64:65], v[184:185], 0, v[112:113]
	global_load_dwordx4 v[96:99], v[64:65], off
	s_add_i32 s0, s4, 0xa0
	s_ashr_i32 s0, s0, 4
	s_ashr_i32 s1, s0, 31
	s_lshl_b64 s[0:1], s[0:1], 6
	v_lshl_add_u64 v[64:65], s[0:1], 0, v[186:187]
	v_lshlrev_b64 v[110:111], 10, v[64:65]
	v_lshl_add_u64 v[64:65], v[184:185], 0, v[110:111]
	global_load_dwordx4 v[88:91], v[64:65], off
	s_addk_i32 s4, 0xb0
	v_lshl_add_u64 v[64:65], s[0:1], 0, v[188:189]
	s_ashr_i32 s0, s4, 4
	v_lshlrev_b64 v[108:109], 10, v[64:65]
	s_ashr_i32 s1, s0, 31
	v_lshl_add_u64 v[64:65], v[184:185], 0, v[108:109]
	s_lshl_b64 s[0:1], s[0:1], 6
	global_load_dwordx4 v[80:83], v[64:65], off
	v_lshl_add_u64 v[64:65], s[0:1], 0, v[186:187]
	v_lshlrev_b64 v[106:107], 10, v[64:65]
	v_lshl_add_u64 v[64:65], v[184:185], 0, v[106:107]
	global_load_dwordx4 v[68:71], v[64:65], off
	v_lshl_add_u64 v[64:65], s[0:1], 0, v[188:189]
	v_lshlrev_b64 v[104:105], 10, v[64:65]
	v_lshl_add_u64 v[64:65], v[184:185], 0, v[104:105]
	global_load_dwordx4 v[64:67], v[64:65], off
	s_mov_b64 s[0:1], -1
	s_waitcnt vmcnt(7)
	v_cvt_f32_f16_e32 v128, v116
	v_cvt_f32_f16_sdwa v129, v116 dst_sel:DWORD dst_unused:UNUSED_PAD src0_sel:WORD_1
	v_cvt_f32_f16_e32 v116, v117
	v_cvt_f32_f16_sdwa v117, v117 dst_sel:DWORD dst_unused:UNUSED_PAD src0_sel:WORD_1
	v_pk_fma_f32 v[60:61], v[60:61], v[92:93], v[128:129]
	s_nop 0
	v_cvt_pk_f16_f32 v60, v60, v61
	v_pk_fma_f32 v[62:63], v[62:63], v[94:95], v[116:117]
	s_nop 0
	v_cvt_pk_f16_f32 v61, v62, v63
	v_cvt_f32_f16_e32 v62, v118
	v_cvt_f32_f16_sdwa v63, v118 dst_sel:DWORD dst_unused:UNUSED_PAD src0_sel:WORD_1
	v_pk_fma_f32 v[56:57], v[56:57], v[84:85], v[62:63]
	s_nop 0
	v_cvt_pk_f16_f32 v62, v56, v57
	v_cvt_f32_f16_e32 v56, v119
	v_cvt_f32_f16_sdwa v57, v119 dst_sel:DWORD dst_unused:UNUSED_PAD src0_sel:WORD_1
	v_pk_fma_f32 v[56:57], v[58:59], v[86:87], v[56:57]
	s_nop 0
	v_cvt_pk_f16_f32 v63, v56, v57
	v_lshl_add_u64 v[56:57], s[20:21], 0, v[124:125]
	v_lshl_add_u64 v[56:57], v[56:57], 0, v[212:213]
	global_store_dwordx4 v[56:57], v[60:63], off nt
	s_waitcnt vmcnt(7)
	v_cvt_f32_f16_e32 v56, v120
	v_cvt_f32_f16_sdwa v57, v120 dst_sel:DWORD dst_unused:UNUSED_PAD src0_sel:WORD_1
	v_pk_fma_f32 v[52:53], v[52:53], v[76:77], v[56:57]
	v_cvt_f32_f16_e32 v56, v121
	v_cvt_f32_f16_sdwa v57, v121 dst_sel:DWORD dst_unused:UNUSED_PAD src0_sel:WORD_1
	v_cvt_pk_f16_f32 v52, v52, v53
	v_pk_fma_f32 v[54:55], v[54:55], v[78:79], v[56:57]
	s_nop 0
	v_cvt_pk_f16_f32 v53, v54, v55
	v_cvt_f32_f16_e32 v54, v122
	v_cvt_f32_f16_sdwa v55, v122 dst_sel:DWORD dst_unused:UNUSED_PAD src0_sel:WORD_1
	v_pk_fma_f32 v[48:49], v[48:49], v[72:73], v[54:55]
	s_nop 0
	v_cvt_pk_f16_f32 v54, v48, v49
	v_cvt_f32_f16_e32 v48, v123
	v_cvt_f32_f16_sdwa v49, v123 dst_sel:DWORD dst_unused:UNUSED_PAD src0_sel:WORD_1
	v_pk_fma_f32 v[48:49], v[50:51], v[74:75], v[48:49]
	s_nop 0
	v_cvt_pk_f16_f32 v55, v48, v49
	v_lshl_add_u64 v[48:49], s[20:21], 0, v[126:127]
	v_lshl_add_u64 v[48:49], v[48:49], 0, v[212:213]
	global_store_dwordx4 v[48:49], v[52:55], off nt
	s_waitcnt vmcnt(7)
	v_cvt_f32_f16_e32 v48, v100
	v_cvt_f32_f16_sdwa v49, v100 dst_sel:DWORD dst_unused:UNUSED_PAD src0_sel:WORD_1
	v_pk_fma_f32 v[44:45], v[44:45], v[92:93], v[48:49]
	v_cvt_f32_f16_e32 v48, v101
	v_cvt_f32_f16_sdwa v49, v101 dst_sel:DWORD dst_unused:UNUSED_PAD src0_sel:WORD_1
	v_cvt_pk_f16_f32 v44, v44, v45
	v_pk_fma_f32 v[46:47], v[46:47], v[94:95], v[48:49]
	s_nop 0
	v_cvt_pk_f16_f32 v45, v46, v47
	v_cvt_f32_f16_e32 v46, v102
	v_cvt_f32_f16_sdwa v47, v102 dst_sel:DWORD dst_unused:UNUSED_PAD src0_sel:WORD_1
	v_pk_fma_f32 v[40:41], v[40:41], v[84:85], v[46:47]
	s_nop 0
	v_cvt_pk_f16_f32 v46, v40, v41
	v_cvt_f32_f16_e32 v40, v103
	v_cvt_f32_f16_sdwa v41, v103 dst_sel:DWORD dst_unused:UNUSED_PAD src0_sel:WORD_1
	v_pk_fma_f32 v[40:41], v[42:43], v[86:87], v[40:41]
	s_nop 0
	v_cvt_pk_f16_f32 v47, v40, v41
	v_lshl_add_u64 v[40:41], s[20:21], 0, v[114:115]
	v_lshl_add_u64 v[40:41], v[40:41], 0, v[212:213]
	global_store_dwordx4 v[40:41], v[44:47], off nt
	s_waitcnt vmcnt(7)
	v_cvt_f32_f16_e32 v40, v96
	v_cvt_f32_f16_sdwa v41, v96 dst_sel:DWORD dst_unused:UNUSED_PAD src0_sel:WORD_1
	v_pk_fma_f32 v[36:37], v[36:37], v[76:77], v[40:41]
	v_cvt_f32_f16_e32 v40, v97
	v_cvt_f32_f16_sdwa v41, v97 dst_sel:DWORD dst_unused:UNUSED_PAD src0_sel:WORD_1
	v_cvt_pk_f16_f32 v36, v36, v37
	v_pk_fma_f32 v[38:39], v[38:39], v[78:79], v[40:41]
	s_nop 0
	v_cvt_pk_f16_f32 v37, v38, v39
	v_cvt_f32_f16_e32 v38, v98
	v_cvt_f32_f16_sdwa v39, v98 dst_sel:DWORD dst_unused:UNUSED_PAD src0_sel:WORD_1
	v_pk_fma_f32 v[32:33], v[32:33], v[72:73], v[38:39]
	s_nop 0
	v_cvt_pk_f16_f32 v38, v32, v33
	v_cvt_f32_f16_e32 v32, v99
	v_cvt_f32_f16_sdwa v33, v99 dst_sel:DWORD dst_unused:UNUSED_PAD src0_sel:WORD_1
	v_pk_fma_f32 v[32:33], v[34:35], v[74:75], v[32:33]
	s_nop 0
	v_cvt_pk_f16_f32 v39, v32, v33
	v_lshl_add_u64 v[32:33], s[20:21], 0, v[112:113]
	v_lshl_add_u64 v[32:33], v[32:33], 0, v[212:213]
	global_store_dwordx4 v[32:33], v[36:39], off nt
	s_waitcnt vmcnt(7)
	v_cvt_f32_f16_e32 v32, v88
	v_cvt_f32_f16_sdwa v33, v88 dst_sel:DWORD dst_unused:UNUSED_PAD src0_sel:WORD_1
	v_pk_fma_f32 v[28:29], v[28:29], v[92:93], v[32:33]
	v_cvt_f32_f16_e32 v32, v89
	v_cvt_f32_f16_sdwa v33, v89 dst_sel:DWORD dst_unused:UNUSED_PAD src0_sel:WORD_1
	v_cvt_pk_f16_f32 v28, v28, v29
	v_pk_fma_f32 v[30:31], v[30:31], v[94:95], v[32:33]
	s_nop 0
	v_cvt_pk_f16_f32 v29, v30, v31
	v_cvt_f32_f16_e32 v30, v90
	v_cvt_f32_f16_sdwa v31, v90 dst_sel:DWORD dst_unused:UNUSED_PAD src0_sel:WORD_1
	v_pk_fma_f32 v[24:25], v[24:25], v[84:85], v[30:31]
	s_nop 0
	v_cvt_pk_f16_f32 v30, v24, v25
	v_cvt_f32_f16_e32 v24, v91
	v_cvt_f32_f16_sdwa v25, v91 dst_sel:DWORD dst_unused:UNUSED_PAD src0_sel:WORD_1
	v_pk_fma_f32 v[24:25], v[26:27], v[86:87], v[24:25]
	s_nop 0
	v_cvt_pk_f16_f32 v31, v24, v25
	v_lshl_add_u64 v[24:25], s[20:21], 0, v[110:111]
	v_lshl_add_u64 v[24:25], v[24:25], 0, v[212:213]
	global_store_dwordx4 v[24:25], v[28:31], off nt
	s_waitcnt vmcnt(7)
	v_cvt_f32_f16_e32 v24, v80
	v_cvt_f32_f16_sdwa v25, v80 dst_sel:DWORD dst_unused:UNUSED_PAD src0_sel:WORD_1
	v_pk_fma_f32 v[20:21], v[20:21], v[76:77], v[24:25]
	v_cvt_f32_f16_e32 v24, v81
	v_cvt_f32_f16_sdwa v25, v81 dst_sel:DWORD dst_unused:UNUSED_PAD src0_sel:WORD_1
	v_cvt_pk_f16_f32 v20, v20, v21
	v_pk_fma_f32 v[22:23], v[22:23], v[78:79], v[24:25]
	s_nop 0
	v_cvt_pk_f16_f32 v21, v22, v23
	v_cvt_f32_f16_e32 v22, v82
	v_cvt_f32_f16_sdwa v23, v82 dst_sel:DWORD dst_unused:UNUSED_PAD src0_sel:WORD_1
	v_pk_fma_f32 v[16:17], v[16:17], v[72:73], v[22:23]
	s_nop 0
	v_cvt_pk_f16_f32 v22, v16, v17
	v_cvt_f32_f16_e32 v16, v83
	v_cvt_f32_f16_sdwa v17, v83 dst_sel:DWORD dst_unused:UNUSED_PAD src0_sel:WORD_1
	v_pk_fma_f32 v[16:17], v[18:19], v[74:75], v[16:17]
	s_nop 0
	v_cvt_pk_f16_f32 v23, v16, v17
	v_lshl_add_u64 v[16:17], s[20:21], 0, v[108:109]
	v_lshl_add_u64 v[16:17], v[16:17], 0, v[212:213]
	global_store_dwordx4 v[16:17], v[20:23], off nt
	s_waitcnt vmcnt(7)
	v_cvt_f32_f16_e32 v16, v68
	v_cvt_f32_f16_sdwa v17, v68 dst_sel:DWORD dst_unused:UNUSED_PAD src0_sel:WORD_1
	v_pk_fma_f32 v[12:13], v[12:13], v[92:93], v[16:17]
	v_cvt_f32_f16_e32 v16, v69
	v_cvt_f32_f16_sdwa v17, v69 dst_sel:DWORD dst_unused:UNUSED_PAD src0_sel:WORD_1
	v_cvt_pk_f16_f32 v12, v12, v13
	v_pk_fma_f32 v[14:15], v[14:15], v[94:95], v[16:17]
	s_nop 0
	v_cvt_pk_f16_f32 v13, v14, v15
	v_cvt_f32_f16_e32 v14, v70
	v_cvt_f32_f16_sdwa v15, v70 dst_sel:DWORD dst_unused:UNUSED_PAD src0_sel:WORD_1
	v_pk_fma_f32 v[8:9], v[8:9], v[84:85], v[14:15]
	s_nop 0
	v_cvt_pk_f16_f32 v14, v8, v9
	v_cvt_f32_f16_e32 v8, v71
	v_cvt_f32_f16_sdwa v9, v71 dst_sel:DWORD dst_unused:UNUSED_PAD src0_sel:WORD_1
	v_pk_fma_f32 v[8:9], v[10:11], v[86:87], v[8:9]
	s_nop 0
	v_cvt_pk_f16_f32 v15, v8, v9
	v_lshl_add_u64 v[8:9], s[20:21], 0, v[106:107]
	v_lshl_add_u64 v[8:9], v[8:9], 0, v[212:213]
	global_store_dwordx4 v[8:9], v[12:15], off nt
	s_waitcnt vmcnt(7)
	v_cvt_f32_f16_e32 v8, v64
	v_cvt_f32_f16_sdwa v9, v64 dst_sel:DWORD dst_unused:UNUSED_PAD src0_sel:WORD_1
	v_pk_fma_f32 v[4:5], v[4:5], v[76:77], v[8:9]
	v_cvt_f32_f16_e32 v8, v65
	v_cvt_f32_f16_sdwa v9, v65 dst_sel:DWORD dst_unused:UNUSED_PAD src0_sel:WORD_1
	v_cvt_pk_f16_f32 v4, v4, v5
	v_pk_fma_f32 v[6:7], v[6:7], v[78:79], v[8:9]
	s_nop 0
	v_cvt_pk_f16_f32 v5, v6, v7
	v_cvt_f32_f16_e32 v6, v66
	v_cvt_f32_f16_sdwa v7, v66 dst_sel:DWORD dst_unused:UNUSED_PAD src0_sel:WORD_1
	v_pk_fma_f32 v[0:1], v[0:1], v[72:73], v[6:7]
	s_nop 0
	v_cvt_pk_f16_f32 v6, v0, v1
	v_cvt_f32_f16_e32 v0, v67
	v_cvt_f32_f16_sdwa v1, v67 dst_sel:DWORD dst_unused:UNUSED_PAD src0_sel:WORD_1
	v_pk_fma_f32 v[0:1], v[2:3], v[74:75], v[0:1]
	s_nop 0
	v_cvt_pk_f16_f32 v7, v0, v1
	v_lshl_add_u64 v[0:1], s[20:21], 0, v[104:105]
	v_lshl_add_u64 v[0:1], v[0:1], 0, v[212:213]
	global_store_dwordx4 v[0:1], v[4:7], off nt
	s_cbranch_vccnz .LBB0_1240
	s_andn2_b64 vcc, exec, s[2:3]
	s_cbranch_vccnz .LBB0_1239
	s_barrier
	s_branch .LBB0_1239
